# speedup vs baseline: 1.0807x; 1.0401x over previous
.LBB0_14:
	s_andn2_saveexec_b64 s[12:13], s[12:13]
	s_cbranch_execz .LBB0_16
	v_mov_b32_e32 v0, v2
	v_mov_b32_e32 v1, 0
	s_waitcnt lgkmcnt(0)
	v_lshl_add_u64 v[2:3], v[0:1], 2, s[4:5]
	v_add_co_u32_e32 v2, vcc, 0x2f15300, v2
	s_nop 1
	v_addc_co_u32_e32 v3, vcc, 0, v3, vcc
	global_store_dword v[2:3], v1, off

.LBB1_12:
	v_readlane_b32 s0, v238, 5
	v_readlane_b32 s1, v238, 6
	s_and_b64 s[0:1], s[4:5], s[0:1]
	s_and_saveexec_b64 s[2:3], s[0:1]
	s_cbranch_execz .LBB1_14
	v_cndmask_b32_e64 v7, v17, 23, s[6:7]
	v_min_i32_e32 v2, v7, v13
	v_sub_u32_e32 v4, 47, v2
	v_mul_lo_u32 v4, v4, v2
	v_lshrrev_b32_e32 v5, 31, v4
	v_add_u32_e32 v4, v4, v5
	v_max_i32_e32 v3, v7, v13
	v_lshrrev_b32_e32 v4, 1, v4
	v_not_b32_e32 v2, v2
	v_readlane_b32 s0, v238, 4
	v_add3_u32 v2, v3, v2, v4
	s_and_b32 s0, s0, 7
	v_lshl_or_b32 v8, v2, 3, s0
	s_mul_i32 s1, s0, 0x114
	v_add_u32_e32 v2, s1, v2
	v_readlane_b32 s4, v238, 2
	v_ashrrev_i32_e32 v3, 31, v2
	v_readlane_b32 s5, v238, 3
	s_mov_b32 s0, 0x3000000
	v_mov_b32_e32 v5, 1
	v_lshl_add_u64 v[2:3], v[2:3], 2, s[4:5]
	v_add_co_u32_e32 v2, vcc, s0, v2
	v_sub_f32_e32 v9, v15, v16
	s_nop 0
	v_addc_co_u32_e32 v3, vcc, 0, v3, vcc
	global_atomic_add v2, v[2:3], v5, off sc0
	v_cndmask_b32_e64 v3, v14, v12, s[6:7]
	s_mov_b32 s0, 0x3fb8aa3b
	v_add_u32_e32 v6, v66, v1
	v_mul_f32_e32 v1, 0x3fb8aa3b, v9
	v_sub_f32_e32 v3, v3, v16
	v_fma_f32 v11, v9, s0, -v1
	v_rndne_f32_e32 v12, v1
	v_mul_f32_e32 v14, 0x3fb8aa3b, v3
	v_fmac_f32_e32 v11, 0x32a5705f, v9
	v_sub_f32_e32 v1, v1, v12
	v_fma_f32 v15, v3, s0, -v14
	v_rndne_f32_e32 v16, v14
	v_add_f32_e32 v1, v1, v11
	v_cvt_i32_f32_e32 v12, v12
	v_fmac_f32_e32 v15, 0x32a5705f, v3
	v_sub_f32_e32 v11, v14, v16
	v_exp_f32_e32 v1, v1
	v_add_f32_e32 v11, v11, v15
	v_cvt_i32_f32_e32 v14, v16
	v_exp_f32_e32 v11, v11
	s_mov_b32 s1, 0xc2ce8ed0
	s_mov_b32 s2, 0x42b17218
	v_ldexp_f32 v1, v1, v12
	v_cmp_ngt_f32_e32 vcc, s1, v9
	v_mov_b32_e32 v10, 0x7f800000
	v_ldexp_f32 v11, v11, v14
	v_cndmask_b32_e32 v1, 0, v1, vcc
	v_cmp_nlt_f32_e32 vcc, s2, v9
	v_mov_b64_e32 v[4:5], s[4:5]
	s_movk_i32 s3, 0x40d0
	v_cndmask_b32_e32 v1, v10, v1, vcc
	v_cmp_ngt_f32_e32 vcc, s1, v3
	v_mul_f32_e32 v1, v0, v1
	s_nop 0
	v_cndmask_b32_e32 v9, 0, v11, vcc
	v_cmp_nlt_f32_e32 vcc, s2, v3
	s_nop 1
	v_cndmask_b32_e32 v3, v10, v9, vcc
	v_mul_f32_e32 v9, v0, v3
	v_fma_f32 v0, v0, v3, v1
	v_div_scale_f32 v3, s[0:1], v0, v0, v1
	v_div_scale_f32 v11, s[0:1], v0, v0, v9
	v_rcp_f32_e32 v12, v3
	v_rcp_f32_e32 v14, v11
	v_div_scale_f32 v10, vcc, v1, v0, v1
	v_fma_f32 v16, -v3, v12, 1.0
	v_fma_f32 v17, -v11, v14, 1.0
	v_fmac_f32_e32 v12, v16, v12
	v_div_scale_f32 v15, s[0:1], v9, v0, v9
	v_fmac_f32_e32 v14, v17, v14
	v_mul_f32_e32 v16, v10, v12
	v_mul_f32_e32 v17, v15, v14
	v_fma_f32 v18, -v3, v16, v10
	v_fma_f32 v19, -v11, v17, v15
	v_fmac_f32_e32 v16, v18, v12
	v_fmac_f32_e32 v17, v19, v14
	v_fma_f32 v3, -v3, v16, v10
	v_fma_f32 v10, -v11, v17, v15
	v_div_fmas_f32 v3, v3, v12, v16
	s_mov_b64 vcc, s[0:1]
	v_div_fixup_f32 v1, v3, v0, v1
	v_div_fmas_f32 v3, v10, v14, v17
	v_div_fixup_f32 v3, v3, v0, v9
	v_cmp_lt_i32_e32 vcc, v7, v13
	v_mad_i64_i32 v[4:5], s[0:1], v8, s3, v[4:5]
	s_nop 0
	v_cndmask_b32_e32 v0, v1, v3, vcc
	v_cndmask_b32_e32 v1, v3, v1, vcc
	s_mov_b32 s0, 0x800000
	v_ashrrev_i32_e32 v7, 31, v6
	s_waitcnt vmcnt(0)
	v_ashrrev_i32_e32 v3, 31, v2
	v_lshl_add_u64 v[2:3], v[2:3], 2, v[4:5]
	v_add_co_u32_e32 v2, vcc, s0, v2
	s_nop 1
	v_addc_co_u32_e32 v3, vcc, 0, v3, vcc
	global_store_dword v[2:3], v6, off
	v_lshl_add_u64 v[2:3], v[6:7], 3, s[4:5]
	v_add_co_u32_e32 v2, vcc, 0x48000, v2
	s_nop 1
	v_addc_co_u32_e32 v3, vcc, 0, v3, vcc
	global_store_dwordx2 v[2:3], v[0:1], off

_Z13expert_kernelPKfS0_PKcPf:
	s_load_dwordx2 s[20:21], s[0:1], 0x10
	v_mov_b32_e32 v11, 0
	v_lshlrev_b32_e32 v10, 2, v0
	v_readfirstlane_b32 s26, v0
	s_mov_b64 s[4:5], 0x3000000
	s_mov_b64 s[6:7], 0x1234
	s_waitcnt lgkmcnt(0)
	v_lshl_add_u64 v[2:3], s[20:21], 0, v[10:11]
	v_lshl_add_u64 v[6:7], v[2:3], 0, s[4:5]
	v_lshl_add_u64 v[18:19], v[6:7], 0, s[6:7]
	v_cmp_gt_u32_e64 s[12:13], 20, v0
	global_load_dword v3, v[6:7], off
	global_load_dword v2, v[6:7], off offset:1104
	global_load_dword v8, v[6:7], off offset:2208
	global_load_dword v9, v[6:7], off offset:3312
	global_load_dword v10, v[18:19], off offset:-244
	global_load_dword v12, v[18:19], off offset:860
	global_load_dword v13, v[18:19], off offset:1964
	global_load_dword v14, v[18:19], off offset:3068
	v_mov_b32_e32 v5, 0
	v_mov_b32_e32 v1, 0
	v_mov_b32_e32 v4, 0
	v_mov_b32_e32 v15, 0
	v_mov_b32_e32 v16, 0
	v_mov_b32_e32 v17, 0
	v_mov_b32_e32 v21, 0
	s_and_saveexec_b64 s[4:5], s[12:13]
	global_load_dword v5, v[6:7], off offset:1024
	global_load_dword v11, v[6:7], off offset:2128
	global_load_dword v4, v[6:7], off offset:3232
	global_load_dword v1, v[18:19], off offset:-324
	global_load_dword v16, v[18:19], off offset:780
	global_load_dword v15, v[18:19], off offset:1884
	global_load_dword v21, v[18:19], off offset:2988
	global_load_dword v17, v[18:19], off offset:4092

.LBB3_33:
	s_or_b64 exec, exec, s[4:5]
	s_add_u32 s4, s20, 0x100000
	s_mul_hi_u32 s2, s26, 0xaaaaaaab
	s_addc_u32 s5, s21, 0
	s_lshr_b32 s6, s2, 8
	s_mul_hi_u32 s2, s27, 0x2aaaaaab
	s_mul_i32 s2, s2, 6
	s_sub_i32 s2, s27, s2
	s_waitcnt vmcnt(5)
	v_mov_b32_e32 v2, s2
	v_sub_co_u32_e64 v3, s[2:3], s2, 3
	v_mov_b32_e32 v85, 0
	s_nop 0
	v_cndmask_b32_e64 v2, v3, v2, s[2:3]
	s_and_b64 s[2:3], s[2:3], exec
	s_cselect_b32 s2, s28, s29
	s_mul_i32 s2, s2, 49
	s_add_i32 s2, s2, s6
	s_mul_hi_u32 s3, s2, 3
	s_mul_i32 s2, s2, 3
	v_mov_b32_e32 v3, v85
	v_lshl_add_u64 v[2:3], s[2:3], 0, v[2:3]
	s_add_i32 s2, s27, 4
	s_mul_hi_u32 s6, s2, 0x2aaaaaab
	v_lshlrev_b64 v[2:3], 10, v[2:3]
	s_mul_i32 s3, s6, 6
	v_lshlrev_b32_e32 v84, 4, v92
	v_lshl_add_u64 v[2:3], s[4:5], 0, v[2:3]
	s_sub_i32 s2, s2, s3
	v_lshl_add_u64 v[86:87], v[2:3], 0, v[84:85]
	v_mov_b32_e32 v2, s2
	v_sub_co_u32_e64 v3, s[2:3], s2, 3
	s_nop 1
	v_cndmask_b32_e64 v2, v3, v2, s[2:3]
	s_and_b64 s[2:3], s[2:3], exec
	s_cselect_b32 s2, s28, s29
	s_mul_i32 s2, s2, 49
	s_add_i32 s2, s2, s6
	s_mul_hi_u32 s3, s2, 3
	s_mul_i32 s2, s2, 3
	v_mov_b32_e32 v3, v85
	v_lshl_add_u64 v[2:3], s[2:3], 0, v[2:3]
	s_add_i32 s2, s27, 8
	s_mul_hi_u32 s6, s2, 0x2aaaaaab
	v_lshlrev_b64 v[2:3], 10, v[2:3]
	s_mul_i32 s3, s6, 6
	v_lshl_add_u64 v[2:3], s[4:5], 0, v[2:3]
	s_sub_i32 s2, s2, s3
	v_lshl_add_u64 v[88:89], v[2:3], 0, v[84:85]
	v_mov_b32_e32 v2, s2
	v_sub_co_u32_e64 v3, s[2:3], s2, 3
	s_nop 1
	v_cndmask_b32_e64 v2, v3, v2, s[2:3]
	s_and_b64 s[2:3], s[2:3], exec
	s_cselect_b32 s2, s28, s29
	s_mul_i32 s2, s2, 49
	s_add_i32 s2, s2, s6
	s_mul_hi_u32 s3, s2, 3
	s_mul_i32 s2, s2, 3
	v_mov_b32_e32 v3, v85
	v_lshl_add_u64 v[2:3], s[2:3], 0, v[2:3]
	v_lshlrev_b64 v[2:3], 10, v[2:3]
	v_lshl_add_u64 v[2:3], s[4:5], 0, v[2:3]
	s_and_b32 s2, s26, 0xfffffc0
	v_lshl_add_u64 v[90:91], v[2:3], 0, v[84:85]
	v_lshl_or_b32 v93, s2, 4, v84
	v_readfirstlane_b32 s40, v86
	v_readfirstlane_b32 s41, v87
	v_readfirstlane_b32 s42, v88
	v_readfirstlane_b32 s43, v89
	v_readfirstlane_b32 s44, v90
	v_readfirstlane_b32 s45, v91
	s_lshl_b32 s46, s27, 10
	s_add_u32 s47, s46, 0x1000
	s_add_u32 s48, s46, 0x2000
	s_movk_i32 s50, 0xc00
	s_movk_i32 s51, 0x1800
	s_cmp_ge_u32 s27, 2
	s_cselect_b32 s49, s50, s51
	s_nop 4
	s_andn2_b64 vcc, exec, vcc
	s_mov_b64 s[2:3], -1
	s_cbranch_vccnz .LBB3_35
	s_add_u32 m0, s46, 0x0
	s_nop 0
	global_load_lds_dwordx4 v84, s[40:41]
	s_add_u32 m0, s47, 0x0
	s_nop 0
	global_load_lds_dwordx4 v84, s[42:43]
	s_add_u32 m0, s48, 0x0
	s_nop 0
	global_load_lds_dwordx4 v84, s[44:45]
	s_add_u32 m0, s46, 0x3000
	s_add_u32 s40, s40, 0x1800
	s_addc_u32 s41, s41, 0
	global_load_lds_dwordx4 v84, s[40:41]
	s_add_u32 m0, s47, 0x3000
	s_add_u32 s42, s42, 0x1800
	s_addc_u32 s43, s43, 0
	global_load_lds_dwordx4 v84, s[42:43]
	s_add_u32 m0, s48, 0x3000
	s_add_u32 s44, s44, 0x1800
	s_addc_u32 s45, s45, 0
	global_load_lds_dwordx4 v84, s[44:45]
	s_add_u32 m0, s46, 0xd3c0
	s_add_u32 s40, s40, 0x1800
	s_addc_u32 s41, s41, 0
	global_load_lds_dwordx4 v84, s[40:41]
	s_add_u32 m0, s47, 0xd3c0
	s_add_u32 s42, s42, 0x1800
	s_addc_u32 s43, s43, 0
	global_load_lds_dwordx4 v84, s[42:43]
	s_add_u32 m0, s48, 0xd3c0
	s_add_u32 s44, s44, 0x1800
	s_addc_u32 s45, s45, 0
	global_load_lds_dwordx4 v84, s[44:45]
	s_add_u32 m0, s46, 0x103c0
	s_add_u32 s40, s40, 0x1800
	s_addc_u32 s41, s41, 0
	global_load_lds_dwordx4 v84, s[40:41]
	s_add_u32 m0, s47, 0x103c0
	s_add_u32 s42, s42, 0x1800
	s_addc_u32 s43, s43, 0
	global_load_lds_dwordx4 v84, s[42:43]
	s_add_u32 m0, s48, 0x103c0
	s_add_u32 s44, s44, 0x1800
	s_addc_u32 s45, s45, 0
	global_load_lds_dwordx4 v84, s[44:45]
	s_waitcnt vmcnt(9)
	s_barrier
	s_waitcnt vmcnt(6)
	s_barrier
	s_add_u32 m0, s46, 0x0
	s_add_u32 s40, s40, 0x1800
	s_addc_u32 s41, s41, 0
	global_load_lds_dwordx4 v84, s[40:41]
	s_add_u32 m0, s47, 0x0
	s_add_u32 s42, s42, 0x1800
	s_addc_u32 s43, s43, 0
	global_load_lds_dwordx4 v84, s[42:43]
	s_add_u32 m0, s48, 0x0
	s_add_u32 s44, s44, 0x1800
	s_addc_u32 s45, s45, 0
	global_load_lds_dwordx4 v84, s[44:45]
	s_waitcnt vmcnt(6)
	s_barrier
	s_add_u32 m0, s46, 0x3000
	s_add_u32 s40, s40, 0x1800
	s_addc_u32 s41, s41, 0
	global_load_lds_dwordx4 v84, s[40:41]
	s_add_u32 m0, s47, 0x3000
	s_add_u32 s42, s42, 0x1800
	s_addc_u32 s43, s43, 0
	global_load_lds_dwordx4 v84, s[42:43]
	s_add_u32 m0, s48, 0x3000
	s_add_u32 s44, s44, 0x1800
	s_addc_u32 s45, s45, 0
	global_load_lds_dwordx4 v84, s[44:45]
	s_waitcnt vmcnt(6)
	s_barrier
	s_add_u32 m0, s46, 0xd3c0
	s_add_u32 s40, s40, 0x1800
	s_addc_u32 s41, s41, 0
	global_load_lds_dwordx4 v84, s[40:41]
	s_add_u32 m0, s47, 0xd3c0
	s_add_u32 s42, s42, 0x1800
	s_addc_u32 s43, s43, 0
	global_load_lds_dwordx4 v84, s[42:43]
	s_add_u32 m0, s48, 0xd3c0
	s_add_u32 s44, s44, 0x1800
	s_addc_u32 s45, s45, 0
	global_load_lds_dwordx4 v84, s[44:45]
	s_waitcnt vmcnt(6)
	s_barrier
	s_add_u32 m0, s46, 0x103c0
	s_add_u32 s40, s40, 0x1800
	s_addc_u32 s41, s41, 0
	global_load_lds_dwordx4 v84, s[40:41]
	s_add_u32 m0, s47, 0x103c0
	s_add_u32 s42, s42, 0x1800
	s_addc_u32 s43, s43, 0
	global_load_lds_dwordx4 v84, s[42:43]
	s_add_u32 m0, s48, 0x103c0
	s_add_u32 s44, s44, 0x1800
	s_addc_u32 s45, s45, 0
	global_load_lds_dwordx4 v84, s[44:45]
	s_waitcnt vmcnt(6)
	s_barrier
	s_add_u32 m0, s46, 0x0
	s_add_u32 s40, s40, 0x1800
	s_addc_u32 s41, s41, 0
	global_load_lds_dwordx4 v84, s[40:41]
	s_add_u32 m0, s47, 0x0
	s_add_u32 s42, s42, 0x1800
	s_addc_u32 s43, s43, 0
	global_load_lds_dwordx4 v84, s[42:43]
	s_add_u32 m0, s48, 0x0
	s_add_u32 s44, s44, 0x1800
	s_addc_u32 s45, s45, 0
	global_load_lds_dwordx4 v84, s[44:45]
	s_waitcnt vmcnt(6)
	s_barrier
	s_add_u32 m0, s46, 0x3000
	s_add_u32 s40, s40, 0x1800
	s_addc_u32 s41, s41, 0
	global_load_lds_dwordx4 v84, s[40:41]
	s_add_u32 m0, s47, 0x3000
	s_add_u32 s42, s42, 0x1800
	s_addc_u32 s43, s43, 0
	global_load_lds_dwordx4 v84, s[42:43]
	s_add_u32 m0, s48, 0x3000
	s_add_u32 s44, s44, 0x1800
	s_addc_u32 s45, s45, 0
	global_load_lds_dwordx4 v84, s[44:45]
	s_waitcnt vmcnt(6)
	s_barrier
	s_add_u32 m0, s46, 0xd3c0
	s_add_u32 s40, s40, 0x1800
	s_addc_u32 s41, s41, 0
	global_load_lds_dwordx4 v84, s[40:41]
	s_add_u32 m0, s47, 0xd3c0
	s_add_u32 s42, s42, 0x1800
	s_addc_u32 s43, s43, 0
	global_load_lds_dwordx4 v84, s[42:43]
	s_add_u32 m0, s48, 0xd3c0
	s_add_u32 s44, s44, 0x1800
	s_addc_u32 s45, s45, 0
	global_load_lds_dwordx4 v84, s[44:45]
	s_waitcnt vmcnt(6)
	s_barrier
	s_add_u32 m0, s46, 0x103c0
	s_add_u32 s40, s40, 0x1800
	s_addc_u32 s41, s41, 0
	global_load_lds_dwordx4 v84, s[40:41]
	s_add_u32 m0, s47, 0x103c0
	s_add_u32 s42, s42, 0x1800
	s_addc_u32 s43, s43, 0
	global_load_lds_dwordx4 v84, s[42:43]
	s_add_u32 m0, s48, 0x103c0
	s_add_u32 s44, s44, 0x1800
	s_addc_u32 s45, s45, 0
	global_load_lds_dwordx4 v84, s[44:45]
	s_waitcnt vmcnt(6)
	s_barrier
	s_add_u32 m0, s46, 0x0
	s_add_u32 s40, s40, 0x1800
	s_addc_u32 s41, s41, 0
	global_load_lds_dwordx4 v84, s[40:41]
	s_add_u32 m0, s47, 0x0
	s_add_u32 s42, s42, 0x1800
	s_addc_u32 s43, s43, 0
	global_load_lds_dwordx4 v84, s[42:43]
	s_add_u32 m0, s48, 0x0
	s_add_u32 s44, s44, 0x1800
	s_addc_u32 s45, s45, 0
	global_load_lds_dwordx4 v84, s[44:45]
	s_waitcnt vmcnt(6)
	s_barrier
	s_add_u32 m0, s46, 0x3000
	s_add_u32 s40, s40, 0x1800
	s_addc_u32 s41, s41, 0
	global_load_lds_dwordx4 v84, s[40:41]
	s_add_u32 m0, s47, 0x3000
	s_add_u32 s42, s42, 0x1800
	s_addc_u32 s43, s43, 0
	global_load_lds_dwordx4 v84, s[42:43]
	s_add_u32 m0, s48, 0x3000
	s_add_u32 s44, s44, 0x1800
	s_addc_u32 s45, s45, 0
	global_load_lds_dwordx4 v84, s[44:45]
	s_waitcnt vmcnt(6)
	s_barrier
	s_add_u32 m0, s46, 0xd3c0
	s_add_u32 s40, s40, 0x1800
	s_addc_u32 s41, s41, 0
	global_load_lds_dwordx4 v84, s[40:41]
	s_add_u32 m0, s47, 0xd3c0
	s_add_u32 s42, s42, 0x1800
	s_addc_u32 s43, s43, 0
	global_load_lds_dwordx4 v84, s[42:43]
	s_add_u32 m0, s48, 0xd3c0
	s_add_u32 s44, s44, 0x1800
	s_addc_u32 s45, s45, 0
	global_load_lds_dwordx4 v84, s[44:45]
	s_waitcnt vmcnt(6)
	s_barrier
	s_add_u32 m0, s46, 0x103c0
	s_add_u32 s40, s40, 0x1800
	s_addc_u32 s41, s41, 0
	global_load_lds_dwordx4 v84, s[40:41]
	s_add_u32 m0, s47, 0x103c0
	s_add_u32 s42, s42, 0x1800
	s_addc_u32 s43, s43, 0
	global_load_lds_dwordx4 v84, s[42:43]
	s_add_u32 m0, s48, 0x103c0
	s_add_u32 s44, s44, 0x1800
	s_addc_u32 s45, s45, 0
	global_load_lds_dwordx4 v84, s[44:45]
	s_waitcnt vmcnt(6)
	s_barrier
	s_add_u32 m0, s46, 0x0
	s_add_u32 s40, s40, 0x1800
	s_addc_u32 s41, s41, 0
	global_load_lds_dwordx4 v84, s[40:41]
	s_add_u32 m0, s47, 0x0
	s_add_u32 s42, s42, 0x1800
	s_addc_u32 s43, s43, 0
	global_load_lds_dwordx4 v84, s[42:43]
	s_add_u32 m0, s48, 0x0
	s_add_u32 s44, s44, 0x1800
	s_addc_u32 s45, s45, 0
	global_load_lds_dwordx4 v84, s[44:45]
	s_waitcnt vmcnt(6)
	s_barrier
	s_add_u32 m0, s46, 0x3000
	s_add_u32 s40, s40, 0x1800
	s_addc_u32 s41, s41, 0
	global_load_lds_dwordx4 v84, s[40:41]
	s_add_u32 m0, s47, 0x3000
	s_add_u32 s42, s42, 0x1800
	s_addc_u32 s43, s43, 0
	global_load_lds_dwordx4 v84, s[42:43]
	s_add_u32 m0, s48, 0x3000
	s_add_u32 s44, s44, 0x1800
	s_addc_u32 s45, s45, 0
	global_load_lds_dwordx4 v84, s[44:45]
	s_waitcnt vmcnt(6)
	s_barrier
	s_add_u32 m0, s46, 0xd3c0
	s_add_u32 s40, s40, 0x1800
	s_addc_u32 s41, s41, 0
	global_load_lds_dwordx4 v84, s[40:41]
	s_add_u32 m0, s47, 0xd3c0
	s_add_u32 s42, s42, 0x1800
	s_addc_u32 s43, s43, 0
	global_load_lds_dwordx4 v84, s[42:43]
	s_add_u32 m0, s48, 0xd3c0
	s_add_u32 s44, s44, 0x1800
	s_addc_u32 s45, s45, 0
	global_load_lds_dwordx4 v84, s[44:45]
	s_waitcnt vmcnt(6)
	s_barrier
	s_add_u32 m0, s46, 0x103c0
	s_add_u32 s40, s40, 0x1800
	s_addc_u32 s41, s41, 0
	global_load_lds_dwordx4 v84, s[40:41]
	s_add_u32 m0, s47, 0x103c0
	s_add_u32 s42, s42, 0x1800
	s_addc_u32 s43, s43, 0
	global_load_lds_dwordx4 v84, s[42:43]
	s_add_u32 m0, s48, 0x103c0
	s_add_u32 s44, s44, 0x1800
	s_addc_u32 s45, s45, 0
	global_load_lds_dwordx4 v84, s[44:45]
	s_waitcnt vmcnt(6)
	s_barrier
	s_add_u32 m0, s46, 0x0
	s_add_u32 s40, s40, 0x1800
	s_addc_u32 s41, s41, 0
	global_load_lds_dwordx4 v84, s[40:41]
	s_add_u32 m0, s47, 0x0
	s_add_u32 s42, s42, 0x1800
	s_addc_u32 s43, s43, 0
	global_load_lds_dwordx4 v84, s[42:43]
	s_add_u32 m0, s48, 0x0
	s_add_u32 s44, s44, 0x1800
	s_addc_u32 s45, s45, 0
	global_load_lds_dwordx4 v84, s[44:45]
	s_waitcnt vmcnt(6)
	s_barrier
	s_add_u32 m0, s46, 0x3000
	s_add_u32 s40, s40, 0x1800
	s_addc_u32 s41, s41, 0
	global_load_lds_dwordx4 v84, s[40:41]
	s_add_u32 m0, s47, 0x3000
	s_add_u32 s42, s42, 0x1800
	s_addc_u32 s43, s43, 0
	global_load_lds_dwordx4 v84, s[42:43]
	s_add_u32 m0, s48, 0x3000
	s_add_u32 s44, s44, 0x1800
	s_addc_u32 s45, s45, 0
	global_load_lds_dwordx4 v84, s[44:45]
	s_waitcnt vmcnt(6)
	s_barrier
	s_add_u32 m0, s46, 0xd3c0
	s_add_u32 s40, s40, 0x1800
	s_addc_u32 s41, s41, 0
	global_load_lds_dwordx4 v84, s[40:41]
	s_add_u32 m0, s47, 0xd3c0
	s_add_u32 s42, s42, 0x1800
	s_addc_u32 s43, s43, 0
	global_load_lds_dwordx4 v84, s[42:43]
	s_add_u32 m0, s48, 0xd3c0
	s_add_u32 s44, s44, 0x1800
	s_addc_u32 s45, s45, 0
	global_load_lds_dwordx4 v84, s[44:45]
	s_waitcnt vmcnt(6)
	s_barrier
	s_add_u32 m0, s46, 0x103c0
	s_add_u32 s40, s40, 0x1800
	s_addc_u32 s41, s41, 0
	global_load_lds_dwordx4 v84, s[40:41]
	s_add_u32 m0, s47, 0x103c0
	s_add_u32 s42, s42, 0x1800
	s_addc_u32 s43, s43, 0
	global_load_lds_dwordx4 v84, s[42:43]
	s_add_u32 m0, s48, 0x103c0
	s_add_u32 s44, s44, 0x1800
	s_addc_u32 s45, s45, 0
	global_load_lds_dwordx4 v84, s[44:45]
	s_waitcnt vmcnt(6)
	s_barrier
	s_add_u32 m0, s46, 0x0
	s_add_u32 s40, s40, 0x1800
	s_addc_u32 s41, s41, 0
	global_load_lds_dwordx4 v84, s[40:41]
	s_add_u32 m0, s47, 0x0
	s_add_u32 s42, s42, s49
	s_addc_u32 s43, s43, 0
	global_load_lds_dwordx4 v84, s[42:43]
	s_add_u32 m0, s48, 0x0
	s_add_u32 s44, s44, 0xc00
	s_addc_u32 s45, s45, 0
	global_load_lds_dwordx4 v84, s[44:45]
	s_waitcnt vmcnt(6)
	s_barrier
	s_waitcnt vmcnt(3)
	s_barrier
	s_waitcnt vmcnt(0)
	s_barrier
	s_branch .LBB3_39
.LBB3_35:
	s_andn2_b64 vcc, exec, s[2:3]
	s_cbranch_vccnz .LBB3_39
	s_waitcnt vmcnt(4)
	v_ashrrev_i32_e32 v81, 31, v80
	v_lshl_add_u64 v[2:3], v[80:81], 3, s[20:21]
	v_add_co_u32_e32 v2, vcc, 0x48000, v2
	s_movk_i32 s8, 0x620
	s_nop 0
	v_addc_co_u32_e32 v3, vcc, 0, v3, vcc
	global_load_dwordx2 v[82:83], v[2:3], off
	v_and_b32_e32 v2, 0x70, v7
	v_bitop3_b32 v2, v0, v2, 48 bitop3:0x6c
	s_waitcnt vmcnt(4)
	v_mad_u64_u32 v[64:65], s[6:7], v9, s8, v[2:3]
	v_lshrrev_b32_e32 v3, 4, v92
	v_bitop3_b32 v3, v3, v0, 4 bitop3:0x36
	v_lshlrev_b32_e32 v3, 4, v3
	v_and_b32_e32 v4, 0x70, v3
	s_waitcnt vmcnt(3)
	v_mad_u64_u32 v[66:67], s[6:7], v8, s8, v[4:5]
	s_waitcnt vmcnt(2)
	v_mad_u64_u32 v[68:69], s[6:7], v6, s8, v[2:3]
	s_waitcnt vmcnt(1)
	v_mad_u64_u32 v[70:71], s[6:7], v1, s8, v[4:5]
	v_lshrrev_b32_e32 v85, 5, v92
	v_bfe_u32 v2, v0, 1, 3
	s_mov_b64 s[6:7], 0x1800
	s_add_u32 s4, s20, 0x4000000
	v_bitop3_b32 v32, v85, v2, 2 bitop3:0x36
	v_bitop3_b32 v33, v85, v2, 4 bitop3:0x36
	v_bitop3_b32 v34, v85, v2, 6 bitop3:0x36
	v_lshl_add_u64 v[2:3], v[86:87], 0, s[6:7]
	s_addc_u32 s5, s21, 0
	s_lshl_b32 s2, s27, 12
	s_addk_i32 s2, 0x6000
	v_lshrrev_b32_e32 v1, 1, v0
	v_or_b32_e32 v81, s2, v84
	v_lshlrev_b32_e32 v0, 7, v0
	v_and_b32_e32 v8, 0xf80, v0
	v_lshlrev_b32_e32 v9, 4, v32
	v_bitop3_b32 v1, v85, v1, 7 bitop3:0x78
	v_or3_b32 v96, s2, v9, v8
	v_lshlrev_b32_e32 v9, 4, v33
	v_lshlrev_b32_e32 v1, 4, v1
	v_or3_b32 v97, s2, v9, v8
	v_lshlrev_b32_e32 v9, 4, v34
	v_or3_b32 v95, s2, v1, v8
	v_or3_b32 v94, s2, v9, v8
	v_add_u32_e32 v98, 0x103c0, v84
	global_load_dwordx4 v[116:119], v64, s[4:5] offset:0
	global_load_dwordx4 v[120:123], v66, s[4:5] offset:0
	global_load_dwordx4 v[124:127], v68, s[4:5] offset:0
	global_load_dwordx4 v[128:131], v70, s[4:5] offset:0
	global_load_dwordx4 v[132:135], v64, s[4:5] offset:128
	global_load_dwordx4 v[136:139], v66, s[4:5] offset:128
	global_load_dwordx4 v[140:143], v68, s[4:5] offset:128
	global_load_dwordx4 v[144:147], v70, s[4:5] offset:128
	global_load_dwordx4 v[148:151], v64, s[4:5] offset:256
	global_load_dwordx4 v[152:155], v66, s[4:5] offset:256
	global_load_dwordx4 v[156:159], v68, s[4:5] offset:256
	global_load_dwordx4 v[72:75], v70, s[4:5] offset:256
	s_add_u32 m0, s46, 0x0
	s_nop 0
	global_load_lds_dwordx4 v84, s[40:41]
	s_add_u32 m0, s47, 0x0
	s_nop 0
	global_load_lds_dwordx4 v84, s[42:43]
	s_add_u32 m0, s48, 0x0
	s_nop 0
	global_load_lds_dwordx4 v84, s[44:45]
	s_add_u32 m0, s46, 0x3000
	s_add_u32 s40, s40, 0x1800
	s_addc_u32 s41, s41, 0
	global_load_lds_dwordx4 v84, s[40:41]
	s_add_u32 m0, s47, 0x3000
	s_add_u32 s42, s42, 0x1800
	s_addc_u32 s43, s43, 0
	global_load_lds_dwordx4 v84, s[42:43]
	s_add_u32 m0, s48, 0x3000
	s_add_u32 s44, s44, 0x1800
	s_addc_u32 s45, s45, 0
	global_load_lds_dwordx4 v84, s[44:45]
	s_add_u32 m0, s46, 0xd3c0
	s_add_u32 s40, s40, 0x1800
	s_addc_u32 s41, s41, 0
	global_load_lds_dwordx4 v84, s[40:41]
	s_add_u32 m0, s47, 0xd3c0
	s_add_u32 s42, s42, 0x1800
	s_addc_u32 s43, s43, 0
	global_load_lds_dwordx4 v84, s[42:43]
	s_add_u32 m0, s48, 0xd3c0
	s_add_u32 s44, s44, 0x1800
	s_addc_u32 s45, s45, 0
	global_load_lds_dwordx4 v84, s[44:45]
	s_add_u32 m0, s46, 0x103c0
	s_add_u32 s40, s40, 0x1800
	s_addc_u32 s41, s41, 0
	global_load_lds_dwordx4 v84, s[40:41]
	s_add_u32 m0, s47, 0x103c0
	s_add_u32 s42, s42, 0x1800
	s_addc_u32 s43, s43, 0
	global_load_lds_dwordx4 v84, s[42:43]
	s_add_u32 m0, s48, 0x103c0
	s_add_u32 s44, s44, 0x1800
	s_addc_u32 s45, s45, 0
	global_load_lds_dwordx4 v84, s[44:45]
	s_waitcnt vmcnt(20)
	ds_write_b128 v81, v[116:119]
	ds_write_b128 v81, v[120:123] offset:1024
	ds_write_b128 v81, v[124:127] offset:2048
	ds_write_b128 v81, v[128:131] offset:3072
	ds_read_b128 v[52:55], v95
	ds_read_b128 v[56:59], v96
	ds_read_b128 v[60:63], v97
	ds_read_b128 v[0:3], v94
	global_load_dwordx4 v[116:119], v64, s[4:5] offset:384
	global_load_dwordx4 v[120:123], v66, s[4:5] offset:384
	global_load_dwordx4 v[124:127], v68, s[4:5] offset:384
	global_load_dwordx4 v[128:131], v70, s[4:5] offset:384
	s_waitcnt vmcnt(13)
	s_waitcnt lgkmcnt(0)
	s_barrier
	ds_read_b128 v[4:7], v84 offset:0
	ds_read_b128 v[8:11], v84 offset:1024
	ds_read_b128 v[12:15], v84 offset:2048
	ds_read_b128 v[16:19], v84 offset:3072
	ds_read_b128 v[20:23], v84 offset:4096
	ds_read_b128 v[24:27], v84 offset:5120
	ds_read_b128 v[28:31], v84 offset:6144
	ds_read_b128 v[32:35], v84 offset:7168
	ds_read_b128 v[36:39], v84 offset:8192
	ds_read_b128 v[40:43], v84 offset:9216
	ds_read_b128 v[44:47], v84 offset:10240
	ds_read_b128 v[48:51], v84 offset:11264
	s_waitcnt lgkmcnt(6)
	v_mfma_f32_32x32x16_f16 a[80:95], v[4:7], v[52:55], 0
	v_mfma_f32_32x32x16_f16 a[64:79], v[8:11], v[52:55], 0
	v_mfma_f32_32x32x16_f16 a[48:63], v[12:15], v[52:55], 0
	v_mfma_f32_32x32x16_f16 a[32:47], v[16:19], v[52:55], 0
	v_mfma_f32_32x32x16_f16 a[16:31], v[20:23], v[52:55], 0
	v_mfma_f32_32x32x16_f16 a[0:15], v[24:27], v[52:55], 0
	s_waitcnt vmcnt(10)
	s_waitcnt lgkmcnt(0)
	s_barrier
	s_add_u32 m0, s46, 0x0
	s_add_u32 s40, s40, 0x1800
	s_addc_u32 s41, s41, 0
	global_load_lds_dwordx4 v84, s[40:41]
	s_add_u32 m0, s47, 0x0
	s_add_u32 s42, s42, 0x1800
	s_addc_u32 s43, s43, 0
	global_load_lds_dwordx4 v84, s[42:43]
	s_add_u32 m0, s48, 0x0
	s_add_u32 s44, s44, 0x1800
	s_addc_u32 s45, s45, 0
	global_load_lds_dwordx4 v84, s[44:45]
	ds_read_b128 v[4:7], v84 offset:12288
	ds_read_b128 v[8:11], v84 offset:13312
	ds_read_b128 v[12:15], v84 offset:14336
	ds_read_b128 v[16:19], v84 offset:15360
	ds_read_b128 v[20:23], v84 offset:16384
	ds_read_b128 v[24:27], v84 offset:17408
	v_mfma_f32_32x32x16_f16 a[80:95], v[28:31], v[56:59], a[80:95]
	v_mfma_f32_32x32x16_f16 a[64:79], v[32:35], v[56:59], a[64:79]
	v_mfma_f32_32x32x16_f16 a[48:63], v[36:39], v[56:59], a[48:63]
	v_mfma_f32_32x32x16_f16 a[32:47], v[40:43], v[56:59], a[32:47]
	v_mfma_f32_32x32x16_f16 a[16:31], v[44:47], v[56:59], a[16:31]
	v_mfma_f32_32x32x16_f16 a[0:15], v[48:51], v[56:59], a[0:15]
	ds_read_b128 v[28:31], v84 offset:18432
	ds_read_b128 v[32:35], v84 offset:19456
	ds_read_b128 v[36:39], v84 offset:20480
	ds_read_b128 v[40:43], v84 offset:21504
	ds_read_b128 v[44:47], v84 offset:22528
	ds_read_b128 v[48:51], v84 offset:23552
	s_waitcnt lgkmcnt(6)
	v_mfma_f32_32x32x16_f16 a[80:95], v[4:7], v[60:63], a[80:95]
	v_mfma_f32_32x32x16_f16 a[64:79], v[8:11], v[60:63], a[64:79]
	v_mfma_f32_32x32x16_f16 a[48:63], v[12:15], v[60:63], a[48:63]
	v_mfma_f32_32x32x16_f16 a[32:47], v[16:19], v[60:63], a[32:47]
	v_mfma_f32_32x32x16_f16 a[16:31], v[20:23], v[60:63], a[16:31]
	v_mfma_f32_32x32x16_f16 a[0:15], v[24:27], v[60:63], a[0:15]
	s_waitcnt vmcnt(23)
	ds_write_b128 v81, v[132:135]
	ds_write_b128 v81, v[136:139] offset:1024
	ds_write_b128 v81, v[140:143] offset:2048
	ds_write_b128 v81, v[144:147] offset:3072
	ds_read_b128 v[100:103], v95
	ds_read_b128 v[104:107], v96
	ds_read_b128 v[108:111], v97
	ds_read_b128 v[112:115], v94
	global_load_dwordx4 v[132:135], v64, s[4:5] offset:512
	global_load_dwordx4 v[136:139], v66, s[4:5] offset:512
	global_load_dwordx4 v[140:143], v68, s[4:5] offset:512
	global_load_dwordx4 v[144:147], v70, s[4:5] offset:512
	s_waitcnt vmcnt(14)
	s_waitcnt lgkmcnt(8)
	s_barrier
	s_add_u32 m0, s46, 0x3000
	s_add_u32 s40, s40, 0x1800
	s_addc_u32 s41, s41, 0
	global_load_lds_dwordx4 v84, s[40:41]
	s_add_u32 m0, s47, 0x3000
	s_add_u32 s42, s42, 0x1800
	s_addc_u32 s43, s43, 0
	global_load_lds_dwordx4 v84, s[42:43]
	s_add_u32 m0, s48, 0x3000
	s_add_u32 s44, s44, 0x1800
	s_addc_u32 s45, s45, 0
	global_load_lds_dwordx4 v84, s[44:45]
	ds_read_b128 v[4:7], v84 offset:54208
	ds_read_b128 v[8:11], v84 offset:55232
	ds_read_b128 v[12:15], v84 offset:56256
	ds_read_b128 v[16:19], v84 offset:57280
	ds_read_b128 v[20:23], v84 offset:58304
	ds_read_b128 v[24:27], v84 offset:59328
	v_mfma_f32_32x32x16_f16 a[80:95], v[28:31], v[0:3], a[80:95]
	v_mfma_f32_32x32x16_f16 a[64:79], v[32:35], v[0:3], a[64:79]
	v_mfma_f32_32x32x16_f16 a[48:63], v[36:39], v[0:3], a[48:63]
	v_mfma_f32_32x32x16_f16 a[32:47], v[40:43], v[0:3], a[32:47]
	v_mfma_f32_32x32x16_f16 a[16:31], v[44:47], v[0:3], a[16:31]
	v_mfma_f32_32x32x16_f16 a[0:15], v[48:51], v[0:3], a[0:15]
	s_waitcnt lgkmcnt(6)
	ds_read_b128 v[28:31], v84 offset:60352
	ds_read_b128 v[32:35], v84 offset:61376
	ds_read_b128 v[36:39], v84 offset:62400
	ds_read_b128 v[40:43], v84 offset:63424
	ds_read_b128 v[44:47], v84 offset:64448
	ds_read_b128 v[48:51], v84 offset:65472
	s_waitcnt lgkmcnt(6)
	v_mfma_f32_32x32x16_f16 a[80:95], v[4:7], v[100:103], a[80:95]
	v_mfma_f32_32x32x16_f16 a[64:79], v[8:11], v[100:103], a[64:79]
	v_mfma_f32_32x32x16_f16 a[48:63], v[12:15], v[100:103], a[48:63]
	v_mfma_f32_32x32x16_f16 a[32:47], v[16:19], v[100:103], a[32:47]
	v_mfma_f32_32x32x16_f16 a[16:31], v[20:23], v[100:103], a[16:31]
	v_mfma_f32_32x32x16_f16 a[0:15], v[24:27], v[100:103], a[0:15]
	s_waitcnt vmcnt(14)
	s_waitcnt lgkmcnt(0)
	s_barrier
	s_add_u32 m0, s46, 0xd3c0
	s_add_u32 s40, s40, 0x1800
	s_addc_u32 s41, s41, 0
	global_load_lds_dwordx4 v84, s[40:41]
	s_add_u32 m0, s47, 0xd3c0
	s_add_u32 s42, s42, 0x1800
	s_addc_u32 s43, s43, 0
	global_load_lds_dwordx4 v84, s[42:43]
	s_add_u32 m0, s48, 0xd3c0
	s_add_u32 s44, s44, 0x1800
	s_addc_u32 s45, s45, 0
	global_load_lds_dwordx4 v84, s[44:45]
	ds_read_b128 v[4:7], v98
	ds_read_b128 v[8:11], v98 offset:1024
	ds_read_b128 v[12:15], v98 offset:2048
	ds_read_b128 v[16:19], v98 offset:3072
	ds_read_b128 v[20:23], v98 offset:4096
	ds_read_b128 v[24:27], v98 offset:5120
	v_mfma_f32_32x32x16_f16 a[80:95], v[28:31], v[104:107], a[80:95]
	v_mfma_f32_32x32x16_f16 a[64:79], v[32:35], v[104:107], a[64:79]
	v_mfma_f32_32x32x16_f16 a[48:63], v[36:39], v[104:107], a[48:63]
	v_mfma_f32_32x32x16_f16 a[32:47], v[40:43], v[104:107], a[32:47]
	v_mfma_f32_32x32x16_f16 a[16:31], v[44:47], v[104:107], a[16:31]
	v_mfma_f32_32x32x16_f16 a[0:15], v[48:51], v[104:107], a[0:15]
	ds_read_b128 v[28:31], v98 offset:6144
	ds_read_b128 v[32:35], v98 offset:7168
	ds_read_b128 v[36:39], v98 offset:8192
	ds_read_b128 v[40:43], v98 offset:9216
	ds_read_b128 v[44:47], v98 offset:10240
	ds_read_b128 v[48:51], v98 offset:11264
	s_waitcnt lgkmcnt(6)
	v_mfma_f32_32x32x16_f16 a[80:95], v[4:7], v[108:111], a[80:95]
	v_mfma_f32_32x32x16_f16 a[64:79], v[8:11], v[108:111], a[64:79]
	v_mfma_f32_32x32x16_f16 a[48:63], v[12:15], v[108:111], a[48:63]
	v_mfma_f32_32x32x16_f16 a[32:47], v[16:19], v[108:111], a[32:47]
	v_mfma_f32_32x32x16_f16 a[16:31], v[20:23], v[108:111], a[16:31]
	v_mfma_f32_32x32x16_f16 a[0:15], v[24:27], v[108:111], a[0:15]
	s_waitcnt vmcnt(29)
	ds_write_b128 v81, v[148:151]
	ds_write_b128 v81, v[152:155] offset:1024
	ds_write_b128 v81, v[156:159] offset:2048
	ds_write_b128 v81, v[72:75] offset:3072
	ds_read_b128 v[52:55], v95
	ds_read_b128 v[56:59], v96
	ds_read_b128 v[60:63], v97
	ds_read_b128 v[0:3], v94
	global_load_dwordx4 v[148:151], v64, s[4:5] offset:640
	global_load_dwordx4 v[152:155], v66, s[4:5] offset:640
	global_load_dwordx4 v[156:159], v68, s[4:5] offset:640
	global_load_dwordx4 v[72:75], v70, s[4:5] offset:640
	s_waitcnt vmcnt(14)
	s_waitcnt lgkmcnt(8)
	s_barrier
	s_add_u32 m0, s46, 0x103c0
	s_add_u32 s40, s40, 0x1800
	s_addc_u32 s41, s41, 0
	global_load_lds_dwordx4 v84, s[40:41]
	s_add_u32 m0, s47, 0x103c0
	s_add_u32 s42, s42, 0x1800
	s_addc_u32 s43, s43, 0
	global_load_lds_dwordx4 v84, s[42:43]
	s_add_u32 m0, s48, 0x103c0
	s_add_u32 s44, s44, 0x1800
	s_addc_u32 s45, s45, 0
	global_load_lds_dwordx4 v84, s[44:45]
	ds_read_b128 v[4:7], v84 offset:0
	ds_read_b128 v[8:11], v84 offset:1024
	ds_read_b128 v[12:15], v84 offset:2048
	ds_read_b128 v[16:19], v84 offset:3072
	ds_read_b128 v[20:23], v84 offset:4096
	ds_read_b128 v[24:27], v84 offset:5120
	v_mfma_f32_32x32x16_f16 a[80:95], v[28:31], v[112:115], a[80:95]
	v_mfma_f32_32x32x16_f16 a[64:79], v[32:35], v[112:115], a[64:79]
	v_mfma_f32_32x32x16_f16 a[48:63], v[36:39], v[112:115], a[48:63]
	v_mfma_f32_32x32x16_f16 a[32:47], v[40:43], v[112:115], a[32:47]
	v_mfma_f32_32x32x16_f16 a[16:31], v[44:47], v[112:115], a[16:31]
	v_mfma_f32_32x32x16_f16 a[0:15], v[48:51], v[112:115], a[0:15]
	s_waitcnt lgkmcnt(6)
	ds_read_b128 v[28:31], v84 offset:6144
	ds_read_b128 v[32:35], v84 offset:7168
	ds_read_b128 v[36:39], v84 offset:8192
	ds_read_b128 v[40:43], v84 offset:9216
	ds_read_b128 v[44:47], v84 offset:10240
	ds_read_b128 v[48:51], v84 offset:11264
	s_waitcnt lgkmcnt(6)
	v_mfma_f32_32x32x16_f16 a[80:95], v[4:7], v[52:55], a[80:95]
	v_mfma_f32_32x32x16_f16 a[64:79], v[8:11], v[52:55], a[64:79]
	v_mfma_f32_32x32x16_f16 a[48:63], v[12:15], v[52:55], a[48:63]
	v_mfma_f32_32x32x16_f16 a[32:47], v[16:19], v[52:55], a[32:47]
	v_mfma_f32_32x32x16_f16 a[16:31], v[20:23], v[52:55], a[16:31]
	v_mfma_f32_32x32x16_f16 a[0:15], v[24:27], v[52:55], a[0:15]
	s_waitcnt vmcnt(10)
	s_waitcnt lgkmcnt(0)
	s_barrier
	s_add_u32 m0, s46, 0x0
	s_add_u32 s40, s40, 0x1800
	s_addc_u32 s41, s41, 0
	global_load_lds_dwordx4 v84, s[40:41]
	s_add_u32 m0, s47, 0x0
	s_add_u32 s42, s42, 0x1800
	s_addc_u32 s43, s43, 0
	global_load_lds_dwordx4 v84, s[42:43]
	s_add_u32 m0, s48, 0x0
	s_add_u32 s44, s44, 0x1800
	s_addc_u32 s45, s45, 0
	global_load_lds_dwordx4 v84, s[44:45]
	ds_read_b128 v[4:7], v84 offset:12288
	ds_read_b128 v[8:11], v84 offset:13312
	ds_read_b128 v[12:15], v84 offset:14336
	ds_read_b128 v[16:19], v84 offset:15360
	ds_read_b128 v[20:23], v84 offset:16384
	ds_read_b128 v[24:27], v84 offset:17408
	v_mfma_f32_32x32x16_f16 a[80:95], v[28:31], v[56:59], a[80:95]
	v_mfma_f32_32x32x16_f16 a[64:79], v[32:35], v[56:59], a[64:79]
	v_mfma_f32_32x32x16_f16 a[48:63], v[36:39], v[56:59], a[48:63]
	v_mfma_f32_32x32x16_f16 a[32:47], v[40:43], v[56:59], a[32:47]
	v_mfma_f32_32x32x16_f16 a[16:31], v[44:47], v[56:59], a[16:31]
	v_mfma_f32_32x32x16_f16 a[0:15], v[48:51], v[56:59], a[0:15]
	ds_read_b128 v[28:31], v84 offset:18432
	ds_read_b128 v[32:35], v84 offset:19456
	ds_read_b128 v[36:39], v84 offset:20480
	ds_read_b128 v[40:43], v84 offset:21504
	ds_read_b128 v[44:47], v84 offset:22528
	ds_read_b128 v[48:51], v84 offset:23552
	s_waitcnt lgkmcnt(6)
	v_mfma_f32_32x32x16_f16 a[80:95], v[4:7], v[60:63], a[80:95]
	v_mfma_f32_32x32x16_f16 a[64:79], v[8:11], v[60:63], a[64:79]
	v_mfma_f32_32x32x16_f16 a[48:63], v[12:15], v[60:63], a[48:63]
	v_mfma_f32_32x32x16_f16 a[32:47], v[16:19], v[60:63], a[32:47]
	v_mfma_f32_32x32x16_f16 a[16:31], v[20:23], v[60:63], a[16:31]
	v_mfma_f32_32x32x16_f16 a[0:15], v[24:27], v[60:63], a[0:15]
	s_waitcnt vmcnt(23)
	ds_write_b128 v81, v[116:119]
	ds_write_b128 v81, v[120:123] offset:1024
	ds_write_b128 v81, v[124:127] offset:2048
	ds_write_b128 v81, v[128:131] offset:3072
	ds_read_b128 v[100:103], v95
	ds_read_b128 v[104:107], v96
	ds_read_b128 v[108:111], v97
	ds_read_b128 v[112:115], v94
	global_load_dwordx4 v[116:119], v64, s[4:5] offset:768
	global_load_dwordx4 v[120:123], v66, s[4:5] offset:768
	global_load_dwordx4 v[124:127], v68, s[4:5] offset:768
	global_load_dwordx4 v[128:131], v70, s[4:5] offset:768
	s_waitcnt vmcnt(14)
	s_waitcnt lgkmcnt(8)
	s_barrier
	s_add_u32 m0, s46, 0x3000
	s_add_u32 s40, s40, 0x1800
	s_addc_u32 s41, s41, 0
	global_load_lds_dwordx4 v84, s[40:41]
	s_add_u32 m0, s47, 0x3000
	s_add_u32 s42, s42, 0x1800
	s_addc_u32 s43, s43, 0
	global_load_lds_dwordx4 v84, s[42:43]
	s_add_u32 m0, s48, 0x3000
	s_add_u32 s44, s44, 0x1800
	s_addc_u32 s45, s45, 0
	global_load_lds_dwordx4 v84, s[44:45]
	ds_read_b128 v[4:7], v84 offset:54208
	ds_read_b128 v[8:11], v84 offset:55232
	ds_read_b128 v[12:15], v84 offset:56256
	ds_read_b128 v[16:19], v84 offset:57280
	ds_read_b128 v[20:23], v84 offset:58304
	ds_read_b128 v[24:27], v84 offset:59328
	v_mfma_f32_32x32x16_f16 a[80:95], v[28:31], v[0:3], a[80:95]
	v_mfma_f32_32x32x16_f16 a[64:79], v[32:35], v[0:3], a[64:79]
	v_mfma_f32_32x32x16_f16 a[48:63], v[36:39], v[0:3], a[48:63]
	v_mfma_f32_32x32x16_f16 a[32:47], v[40:43], v[0:3], a[32:47]
	v_mfma_f32_32x32x16_f16 a[16:31], v[44:47], v[0:3], a[16:31]
	v_mfma_f32_32x32x16_f16 a[0:15], v[48:51], v[0:3], a[0:15]
	s_waitcnt lgkmcnt(6)
	ds_read_b128 v[28:31], v84 offset:60352
	ds_read_b128 v[32:35], v84 offset:61376
	ds_read_b128 v[36:39], v84 offset:62400
	ds_read_b128 v[40:43], v84 offset:63424
	ds_read_b128 v[44:47], v84 offset:64448
	ds_read_b128 v[48:51], v84 offset:65472
	s_waitcnt lgkmcnt(6)
	v_mfma_f32_32x32x16_f16 a[80:95], v[4:7], v[100:103], a[80:95]
	v_mfma_f32_32x32x16_f16 a[64:79], v[8:11], v[100:103], a[64:79]
	v_mfma_f32_32x32x16_f16 a[48:63], v[12:15], v[100:103], a[48:63]
	v_mfma_f32_32x32x16_f16 a[32:47], v[16:19], v[100:103], a[32:47]
	v_mfma_f32_32x32x16_f16 a[16:31], v[20:23], v[100:103], a[16:31]
	v_mfma_f32_32x32x16_f16 a[0:15], v[24:27], v[100:103], a[0:15]
	s_waitcnt vmcnt(10)
	s_waitcnt lgkmcnt(0)
	s_barrier
	s_add_u32 m0, s46, 0xd3c0
	s_add_u32 s40, s40, 0x1800
	s_addc_u32 s41, s41, 0
	global_load_lds_dwordx4 v84, s[40:41]
	s_add_u32 m0, s47, 0xd3c0
	s_add_u32 s42, s42, 0x1800
	s_addc_u32 s43, s43, 0
	global_load_lds_dwordx4 v84, s[42:43]
	s_add_u32 m0, s48, 0xd3c0
	s_add_u32 s44, s44, 0x1800
	s_addc_u32 s45, s45, 0
	global_load_lds_dwordx4 v84, s[44:45]
	ds_read_b128 v[4:7], v98
	ds_read_b128 v[8:11], v98 offset:1024
	ds_read_b128 v[12:15], v98 offset:2048
	ds_read_b128 v[16:19], v98 offset:3072
	ds_read_b128 v[20:23], v98 offset:4096
	ds_read_b128 v[24:27], v98 offset:5120
	v_mfma_f32_32x32x16_f16 a[80:95], v[28:31], v[104:107], a[80:95]
	v_mfma_f32_32x32x16_f16 a[64:79], v[32:35], v[104:107], a[64:79]
	v_mfma_f32_32x32x16_f16 a[48:63], v[36:39], v[104:107], a[48:63]
	v_mfma_f32_32x32x16_f16 a[32:47], v[40:43], v[104:107], a[32:47]
	v_mfma_f32_32x32x16_f16 a[16:31], v[44:47], v[104:107], a[16:31]
	v_mfma_f32_32x32x16_f16 a[0:15], v[48:51], v[104:107], a[0:15]
	ds_read_b128 v[28:31], v98 offset:6144
	ds_read_b128 v[32:35], v98 offset:7168
	ds_read_b128 v[36:39], v98 offset:8192
	ds_read_b128 v[40:43], v98 offset:9216
	ds_read_b128 v[44:47], v98 offset:10240
	ds_read_b128 v[48:51], v98 offset:11264
	s_waitcnt lgkmcnt(6)
	v_mfma_f32_32x32x16_f16 a[80:95], v[4:7], v[108:111], a[80:95]
	v_mfma_f32_32x32x16_f16 a[64:79], v[8:11], v[108:111], a[64:79]
	v_mfma_f32_32x32x16_f16 a[48:63], v[12:15], v[108:111], a[48:63]
	v_mfma_f32_32x32x16_f16 a[32:47], v[16:19], v[108:111], a[32:47]
	v_mfma_f32_32x32x16_f16 a[16:31], v[20:23], v[108:111], a[16:31]
	v_mfma_f32_32x32x16_f16 a[0:15], v[24:27], v[108:111], a[0:15]
	s_waitcnt vmcnt(26)
	ds_write_b128 v81, v[132:135]
	ds_write_b128 v81, v[136:139] offset:1024
	ds_write_b128 v81, v[140:143] offset:2048
	ds_write_b128 v81, v[144:147] offset:3072
	ds_read_b128 v[52:55], v95
	ds_read_b128 v[56:59], v96
	ds_read_b128 v[60:63], v97
	ds_read_b128 v[0:3], v94
	global_load_dwordx4 v[132:135], v64, s[4:5] offset:896
	global_load_dwordx4 v[136:139], v66, s[4:5] offset:896
	global_load_dwordx4 v[140:143], v68, s[4:5] offset:896
	global_load_dwordx4 v[144:147], v70, s[4:5] offset:896
	s_waitcnt vmcnt(14)
	s_waitcnt lgkmcnt(8)
	s_barrier
	s_add_u32 m0, s46, 0x103c0
	s_add_u32 s40, s40, 0x1800
	s_addc_u32 s41, s41, 0
	global_load_lds_dwordx4 v84, s[40:41]
	s_add_u32 m0, s47, 0x103c0
	s_add_u32 s42, s42, 0x1800
	s_addc_u32 s43, s43, 0
	global_load_lds_dwordx4 v84, s[42:43]
	s_add_u32 m0, s48, 0x103c0
	s_add_u32 s44, s44, 0x1800
	s_addc_u32 s45, s45, 0
	global_load_lds_dwordx4 v84, s[44:45]
	ds_read_b128 v[4:7], v84 offset:0
	ds_read_b128 v[8:11], v84 offset:1024
	ds_read_b128 v[12:15], v84 offset:2048
	ds_read_b128 v[16:19], v84 offset:3072
	ds_read_b128 v[20:23], v84 offset:4096
	ds_read_b128 v[24:27], v84 offset:5120
	v_mfma_f32_32x32x16_f16 a[80:95], v[28:31], v[112:115], a[80:95]
	v_mfma_f32_32x32x16_f16 a[64:79], v[32:35], v[112:115], a[64:79]
	v_mfma_f32_32x32x16_f16 a[48:63], v[36:39], v[112:115], a[48:63]
	v_mfma_f32_32x32x16_f16 a[32:47], v[40:43], v[112:115], a[32:47]
	v_mfma_f32_32x32x16_f16 a[16:31], v[44:47], v[112:115], a[16:31]
	v_mfma_f32_32x32x16_f16 a[0:15], v[48:51], v[112:115], a[0:15]
	s_waitcnt lgkmcnt(6)
	ds_read_b128 v[28:31], v84 offset:6144
	ds_read_b128 v[32:35], v84 offset:7168
	ds_read_b128 v[36:39], v84 offset:8192
	ds_read_b128 v[40:43], v84 offset:9216
	ds_read_b128 v[44:47], v84 offset:10240
	ds_read_b128 v[48:51], v84 offset:11264
	s_waitcnt lgkmcnt(6)
	v_mfma_f32_32x32x16_f16 a[80:95], v[4:7], v[52:55], a[80:95]
	v_mfma_f32_32x32x16_f16 a[64:79], v[8:11], v[52:55], a[64:79]
	v_mfma_f32_32x32x16_f16 a[48:63], v[12:15], v[52:55], a[48:63]
	v_mfma_f32_32x32x16_f16 a[32:47], v[16:19], v[52:55], a[32:47]
	v_mfma_f32_32x32x16_f16 a[16:31], v[20:23], v[52:55], a[16:31]
	v_mfma_f32_32x32x16_f16 a[0:15], v[24:27], v[52:55], a[0:15]
	s_waitcnt vmcnt(10)
	s_waitcnt lgkmcnt(0)
	s_barrier
	s_add_u32 m0, s46, 0x0
	s_add_u32 s40, s40, 0x1800
	s_addc_u32 s41, s41, 0
	global_load_lds_dwordx4 v84, s[40:41]
	s_add_u32 m0, s47, 0x0
	s_add_u32 s42, s42, 0x1800
	s_addc_u32 s43, s43, 0
	global_load_lds_dwordx4 v84, s[42:43]
	s_add_u32 m0, s48, 0x0
	s_add_u32 s44, s44, 0x1800
	s_addc_u32 s45, s45, 0
	global_load_lds_dwordx4 v84, s[44:45]
	ds_read_b128 v[4:7], v84 offset:12288
	ds_read_b128 v[8:11], v84 offset:13312
	ds_read_b128 v[12:15], v84 offset:14336
	ds_read_b128 v[16:19], v84 offset:15360
	ds_read_b128 v[20:23], v84 offset:16384
	ds_read_b128 v[24:27], v84 offset:17408
	v_mfma_f32_32x32x16_f16 a[80:95], v[28:31], v[56:59], a[80:95]
	v_mfma_f32_32x32x16_f16 a[64:79], v[32:35], v[56:59], a[64:79]
	v_mfma_f32_32x32x16_f16 a[48:63], v[36:39], v[56:59], a[48:63]
	v_mfma_f32_32x32x16_f16 a[32:47], v[40:43], v[56:59], a[32:47]
	v_mfma_f32_32x32x16_f16 a[16:31], v[44:47], v[56:59], a[16:31]
	v_mfma_f32_32x32x16_f16 a[0:15], v[48:51], v[56:59], a[0:15]
	ds_read_b128 v[28:31], v84 offset:18432
	ds_read_b128 v[32:35], v84 offset:19456
	ds_read_b128 v[36:39], v84 offset:20480
	ds_read_b128 v[40:43], v84 offset:21504
	ds_read_b128 v[44:47], v84 offset:22528
	ds_read_b128 v[48:51], v84 offset:23552
	s_waitcnt lgkmcnt(6)
	v_mfma_f32_32x32x16_f16 a[80:95], v[4:7], v[60:63], a[80:95]
	v_mfma_f32_32x32x16_f16 a[64:79], v[8:11], v[60:63], a[64:79]
	v_mfma_f32_32x32x16_f16 a[48:63], v[12:15], v[60:63], a[48:63]
	v_mfma_f32_32x32x16_f16 a[32:47], v[16:19], v[60:63], a[32:47]
	v_mfma_f32_32x32x16_f16 a[16:31], v[20:23], v[60:63], a[16:31]
	v_mfma_f32_32x32x16_f16 a[0:15], v[24:27], v[60:63], a[0:15]
	s_waitcnt vmcnt(26)
	ds_write_b128 v81, v[148:151]
	ds_write_b128 v81, v[152:155] offset:1024
	ds_write_b128 v81, v[156:159] offset:2048
	ds_write_b128 v81, v[72:75] offset:3072
	ds_read_b128 v[100:103], v95
	ds_read_b128 v[104:107], v96
	ds_read_b128 v[108:111], v97
	ds_read_b128 v[112:115], v94
	global_load_dwordx4 v[148:151], v64, s[4:5] offset:1024
	global_load_dwordx4 v[152:155], v66, s[4:5] offset:1024
	global_load_dwordx4 v[156:159], v68, s[4:5] offset:1024
	global_load_dwordx4 v[72:75], v70, s[4:5] offset:1024
	s_waitcnt vmcnt(14)
	s_waitcnt lgkmcnt(8)
	s_barrier
	s_add_u32 m0, s46, 0x3000
	s_add_u32 s40, s40, 0x1800
	s_addc_u32 s41, s41, 0
	global_load_lds_dwordx4 v84, s[40:41]
	s_add_u32 m0, s47, 0x3000
	s_add_u32 s42, s42, 0x1800
	s_addc_u32 s43, s43, 0
	global_load_lds_dwordx4 v84, s[42:43]
	s_add_u32 m0, s48, 0x3000
	s_add_u32 s44, s44, 0x1800
	s_addc_u32 s45, s45, 0
	global_load_lds_dwordx4 v84, s[44:45]
	ds_read_b128 v[4:7], v84 offset:54208
	ds_read_b128 v[8:11], v84 offset:55232
	ds_read_b128 v[12:15], v84 offset:56256
	ds_read_b128 v[16:19], v84 offset:57280
	ds_read_b128 v[20:23], v84 offset:58304
	ds_read_b128 v[24:27], v84 offset:59328
	v_mfma_f32_32x32x16_f16 a[80:95], v[28:31], v[0:3], a[80:95]
	v_mfma_f32_32x32x16_f16 a[64:79], v[32:35], v[0:3], a[64:79]
	v_mfma_f32_32x32x16_f16 a[48:63], v[36:39], v[0:3], a[48:63]
	v_mfma_f32_32x32x16_f16 a[32:47], v[40:43], v[0:3], a[32:47]
	v_mfma_f32_32x32x16_f16 a[16:31], v[44:47], v[0:3], a[16:31]
	v_mfma_f32_32x32x16_f16 a[0:15], v[48:51], v[0:3], a[0:15]
	s_waitcnt lgkmcnt(6)
	ds_read_b128 v[28:31], v84 offset:60352
	ds_read_b128 v[32:35], v84 offset:61376
	ds_read_b128 v[36:39], v84 offset:62400
	ds_read_b128 v[40:43], v84 offset:63424
	ds_read_b128 v[44:47], v84 offset:64448
	ds_read_b128 v[48:51], v84 offset:65472
	s_waitcnt lgkmcnt(6)
	v_mfma_f32_32x32x16_f16 a[80:95], v[4:7], v[100:103], a[80:95]
	v_mfma_f32_32x32x16_f16 a[64:79], v[8:11], v[100:103], a[64:79]
	v_mfma_f32_32x32x16_f16 a[48:63], v[12:15], v[100:103], a[48:63]
	v_mfma_f32_32x32x16_f16 a[32:47], v[16:19], v[100:103], a[32:47]
	v_mfma_f32_32x32x16_f16 a[16:31], v[20:23], v[100:103], a[16:31]
	v_mfma_f32_32x32x16_f16 a[0:15], v[24:27], v[100:103], a[0:15]
	s_waitcnt vmcnt(10)
	s_waitcnt lgkmcnt(0)
	s_barrier
	s_add_u32 m0, s46, 0xd3c0
	s_add_u32 s40, s40, 0x1800
	s_addc_u32 s41, s41, 0
	global_load_lds_dwordx4 v84, s[40:41]
	s_add_u32 m0, s47, 0xd3c0
	s_add_u32 s42, s42, 0x1800
	s_addc_u32 s43, s43, 0
	global_load_lds_dwordx4 v84, s[42:43]
	s_add_u32 m0, s48, 0xd3c0
	s_add_u32 s44, s44, 0x1800
	s_addc_u32 s45, s45, 0
	global_load_lds_dwordx4 v84, s[44:45]
	ds_read_b128 v[4:7], v98
	ds_read_b128 v[8:11], v98 offset:1024
	ds_read_b128 v[12:15], v98 offset:2048
	ds_read_b128 v[16:19], v98 offset:3072
	ds_read_b128 v[20:23], v98 offset:4096
	ds_read_b128 v[24:27], v98 offset:5120
	v_mfma_f32_32x32x16_f16 a[80:95], v[28:31], v[104:107], a[80:95]
	v_mfma_f32_32x32x16_f16 a[64:79], v[32:35], v[104:107], a[64:79]
	v_mfma_f32_32x32x16_f16 a[48:63], v[36:39], v[104:107], a[48:63]
	v_mfma_f32_32x32x16_f16 a[32:47], v[40:43], v[104:107], a[32:47]
	v_mfma_f32_32x32x16_f16 a[16:31], v[44:47], v[104:107], a[16:31]
	v_mfma_f32_32x32x16_f16 a[0:15], v[48:51], v[104:107], a[0:15]
	ds_read_b128 v[28:31], v98 offset:6144
	ds_read_b128 v[32:35], v98 offset:7168
	ds_read_b128 v[36:39], v98 offset:8192
	ds_read_b128 v[40:43], v98 offset:9216
	ds_read_b128 v[44:47], v98 offset:10240
	ds_read_b128 v[48:51], v98 offset:11264
	s_waitcnt lgkmcnt(6)
	v_mfma_f32_32x32x16_f16 a[80:95], v[4:7], v[108:111], a[80:95]
	v_mfma_f32_32x32x16_f16 a[64:79], v[8:11], v[108:111], a[64:79]
	v_mfma_f32_32x32x16_f16 a[48:63], v[12:15], v[108:111], a[48:63]
	v_mfma_f32_32x32x16_f16 a[32:47], v[16:19], v[108:111], a[32:47]
	v_mfma_f32_32x32x16_f16 a[16:31], v[20:23], v[108:111], a[16:31]
	v_mfma_f32_32x32x16_f16 a[0:15], v[24:27], v[108:111], a[0:15]
	s_waitcnt vmcnt(26)
	ds_write_b128 v81, v[116:119]
	ds_write_b128 v81, v[120:123] offset:1024
	ds_write_b128 v81, v[124:127] offset:2048
	ds_write_b128 v81, v[128:131] offset:3072
	ds_read_b128 v[52:55], v95
	ds_read_b128 v[56:59], v96
	ds_read_b128 v[60:63], v97
	ds_read_b128 v[0:3], v94
	global_load_dwordx4 v[116:119], v64, s[4:5] offset:1152
	global_load_dwordx4 v[120:123], v66, s[4:5] offset:1152
	global_load_dwordx4 v[124:127], v68, s[4:5] offset:1152
	global_load_dwordx4 v[128:131], v70, s[4:5] offset:1152
	s_waitcnt vmcnt(14)
	s_waitcnt lgkmcnt(8)
	s_barrier
	s_add_u32 m0, s46, 0x103c0
	s_add_u32 s40, s40, 0x1800
	s_addc_u32 s41, s41, 0
	global_load_lds_dwordx4 v84, s[40:41]
	s_add_u32 m0, s47, 0x103c0
	s_add_u32 s42, s42, 0x1800
	s_addc_u32 s43, s43, 0
	global_load_lds_dwordx4 v84, s[42:43]
	s_add_u32 m0, s48, 0x103c0
	s_add_u32 s44, s44, 0x1800
	s_addc_u32 s45, s45, 0
	global_load_lds_dwordx4 v84, s[44:45]
	ds_read_b128 v[4:7], v84 offset:0
	ds_read_b128 v[8:11], v84 offset:1024
	ds_read_b128 v[12:15], v84 offset:2048
	ds_read_b128 v[16:19], v84 offset:3072
	ds_read_b128 v[20:23], v84 offset:4096
	ds_read_b128 v[24:27], v84 offset:5120
	v_mfma_f32_32x32x16_f16 a[80:95], v[28:31], v[112:115], a[80:95]
	v_mfma_f32_32x32x16_f16 a[64:79], v[32:35], v[112:115], a[64:79]
	v_mfma_f32_32x32x16_f16 a[48:63], v[36:39], v[112:115], a[48:63]
	v_mfma_f32_32x32x16_f16 a[32:47], v[40:43], v[112:115], a[32:47]
	v_mfma_f32_32x32x16_f16 a[16:31], v[44:47], v[112:115], a[16:31]
	v_mfma_f32_32x32x16_f16 a[0:15], v[48:51], v[112:115], a[0:15]
	s_waitcnt lgkmcnt(6)
	ds_read_b128 v[28:31], v84 offset:6144
	ds_read_b128 v[32:35], v84 offset:7168
	ds_read_b128 v[36:39], v84 offset:8192
	ds_read_b128 v[40:43], v84 offset:9216
	ds_read_b128 v[44:47], v84 offset:10240
	ds_read_b128 v[48:51], v84 offset:11264
	s_waitcnt lgkmcnt(6)
	v_mfma_f32_32x32x16_f16 a[80:95], v[4:7], v[52:55], a[80:95]
	v_mfma_f32_32x32x16_f16 a[64:79], v[8:11], v[52:55], a[64:79]
	v_mfma_f32_32x32x16_f16 a[48:63], v[12:15], v[52:55], a[48:63]
	v_mfma_f32_32x32x16_f16 a[32:47], v[16:19], v[52:55], a[32:47]
	v_mfma_f32_32x32x16_f16 a[16:31], v[20:23], v[52:55], a[16:31]
	v_mfma_f32_32x32x16_f16 a[0:15], v[24:27], v[52:55], a[0:15]
	s_waitcnt vmcnt(10)
	s_waitcnt lgkmcnt(0)
	s_barrier
	s_add_u32 m0, s46, 0x0
	s_add_u32 s40, s40, 0x1800
	s_addc_u32 s41, s41, 0
	global_load_lds_dwordx4 v84, s[40:41]
	s_add_u32 m0, s47, 0x0
	s_add_u32 s42, s42, 0x1800
	s_addc_u32 s43, s43, 0
	global_load_lds_dwordx4 v84, s[42:43]
	s_add_u32 m0, s48, 0x0
	s_add_u32 s44, s44, 0x1800
	s_addc_u32 s45, s45, 0
	global_load_lds_dwordx4 v84, s[44:45]
	ds_read_b128 v[4:7], v84 offset:12288
	ds_read_b128 v[8:11], v84 offset:13312
	ds_read_b128 v[12:15], v84 offset:14336
	ds_read_b128 v[16:19], v84 offset:15360
	ds_read_b128 v[20:23], v84 offset:16384
	ds_read_b128 v[24:27], v84 offset:17408
	v_mfma_f32_32x32x16_f16 a[80:95], v[28:31], v[56:59], a[80:95]
	v_mfma_f32_32x32x16_f16 a[64:79], v[32:35], v[56:59], a[64:79]
	v_mfma_f32_32x32x16_f16 a[48:63], v[36:39], v[56:59], a[48:63]
	v_mfma_f32_32x32x16_f16 a[32:47], v[40:43], v[56:59], a[32:47]
	v_mfma_f32_32x32x16_f16 a[16:31], v[44:47], v[56:59], a[16:31]
	v_mfma_f32_32x32x16_f16 a[0:15], v[48:51], v[56:59], a[0:15]
	ds_read_b128 v[28:31], v84 offset:18432
	ds_read_b128 v[32:35], v84 offset:19456
	ds_read_b128 v[36:39], v84 offset:20480
	ds_read_b128 v[40:43], v84 offset:21504
	ds_read_b128 v[44:47], v84 offset:22528
	ds_read_b128 v[48:51], v84 offset:23552
	s_waitcnt lgkmcnt(6)
	v_mfma_f32_32x32x16_f16 a[80:95], v[4:7], v[60:63], a[80:95]
	v_mfma_f32_32x32x16_f16 a[64:79], v[8:11], v[60:63], a[64:79]
	v_mfma_f32_32x32x16_f16 a[48:63], v[12:15], v[60:63], a[48:63]
	v_mfma_f32_32x32x16_f16 a[32:47], v[16:19], v[60:63], a[32:47]
	v_mfma_f32_32x32x16_f16 a[16:31], v[20:23], v[60:63], a[16:31]
	v_mfma_f32_32x32x16_f16 a[0:15], v[24:27], v[60:63], a[0:15]
	s_waitcnt vmcnt(26)
	ds_write_b128 v81, v[132:135]
	ds_write_b128 v81, v[136:139] offset:1024
	ds_write_b128 v81, v[140:143] offset:2048
	ds_write_b128 v81, v[144:147] offset:3072
	ds_read_b128 v[100:103], v95
	ds_read_b128 v[104:107], v96
	ds_read_b128 v[108:111], v97
	ds_read_b128 v[112:115], v94
	global_load_dwordx4 v[132:135], v64, s[4:5] offset:1280
	global_load_dwordx4 v[136:139], v66, s[4:5] offset:1280
	global_load_dwordx4 v[140:143], v68, s[4:5] offset:1280
	global_load_dwordx4 v[144:147], v70, s[4:5] offset:1280
	s_waitcnt vmcnt(14)
	s_waitcnt lgkmcnt(8)
	s_barrier
	s_add_u32 m0, s46, 0x3000
	s_add_u32 s40, s40, 0x1800
	s_addc_u32 s41, s41, 0
	global_load_lds_dwordx4 v84, s[40:41]
	s_add_u32 m0, s47, 0x3000
	s_add_u32 s42, s42, 0x1800
	s_addc_u32 s43, s43, 0
	global_load_lds_dwordx4 v84, s[42:43]
	s_add_u32 m0, s48, 0x3000
	s_add_u32 s44, s44, 0x1800
	s_addc_u32 s45, s45, 0
	global_load_lds_dwordx4 v84, s[44:45]
	ds_read_b128 v[4:7], v84 offset:54208
	ds_read_b128 v[8:11], v84 offset:55232
	ds_read_b128 v[12:15], v84 offset:56256
	ds_read_b128 v[16:19], v84 offset:57280
	ds_read_b128 v[20:23], v84 offset:58304
	ds_read_b128 v[24:27], v84 offset:59328
	v_mfma_f32_32x32x16_f16 a[80:95], v[28:31], v[0:3], a[80:95]
	v_mfma_f32_32x32x16_f16 a[64:79], v[32:35], v[0:3], a[64:79]
	v_mfma_f32_32x32x16_f16 a[48:63], v[36:39], v[0:3], a[48:63]
	v_mfma_f32_32x32x16_f16 a[32:47], v[40:43], v[0:3], a[32:47]
	v_mfma_f32_32x32x16_f16 a[16:31], v[44:47], v[0:3], a[16:31]
	v_mfma_f32_32x32x16_f16 a[0:15], v[48:51], v[0:3], a[0:15]
	s_waitcnt lgkmcnt(6)
	ds_read_b128 v[28:31], v84 offset:60352
	ds_read_b128 v[32:35], v84 offset:61376
	ds_read_b128 v[36:39], v84 offset:62400
	ds_read_b128 v[40:43], v84 offset:63424
	ds_read_b128 v[44:47], v84 offset:64448
	ds_read_b128 v[48:51], v84 offset:65472
	s_waitcnt lgkmcnt(6)
	v_mfma_f32_32x32x16_f16 a[80:95], v[4:7], v[100:103], a[80:95]
	v_mfma_f32_32x32x16_f16 a[64:79], v[8:11], v[100:103], a[64:79]
	v_mfma_f32_32x32x16_f16 a[48:63], v[12:15], v[100:103], a[48:63]
	v_mfma_f32_32x32x16_f16 a[32:47], v[16:19], v[100:103], a[32:47]
	v_mfma_f32_32x32x16_f16 a[16:31], v[20:23], v[100:103], a[16:31]
	v_mfma_f32_32x32x16_f16 a[0:15], v[24:27], v[100:103], a[0:15]
	s_waitcnt vmcnt(10)
	s_waitcnt lgkmcnt(0)
	s_barrier
	s_add_u32 m0, s46, 0xd3c0
	s_add_u32 s40, s40, 0x1800
	s_addc_u32 s41, s41, 0
	global_load_lds_dwordx4 v84, s[40:41]
	s_add_u32 m0, s47, 0xd3c0
	s_add_u32 s42, s42, 0x1800
	s_addc_u32 s43, s43, 0
	global_load_lds_dwordx4 v84, s[42:43]
	s_add_u32 m0, s48, 0xd3c0
	s_add_u32 s44, s44, 0x1800
	s_addc_u32 s45, s45, 0
	global_load_lds_dwordx4 v84, s[44:45]
	ds_read_b128 v[4:7], v98
	ds_read_b128 v[8:11], v98 offset:1024
	ds_read_b128 v[12:15], v98 offset:2048
	ds_read_b128 v[16:19], v98 offset:3072
	ds_read_b128 v[20:23], v98 offset:4096
	ds_read_b128 v[24:27], v98 offset:5120
	v_mfma_f32_32x32x16_f16 a[80:95], v[28:31], v[104:107], a[80:95]
	v_mfma_f32_32x32x16_f16 a[64:79], v[32:35], v[104:107], a[64:79]
	v_mfma_f32_32x32x16_f16 a[48:63], v[36:39], v[104:107], a[48:63]
	v_mfma_f32_32x32x16_f16 a[32:47], v[40:43], v[104:107], a[32:47]
	v_mfma_f32_32x32x16_f16 a[16:31], v[44:47], v[104:107], a[16:31]
	v_mfma_f32_32x32x16_f16 a[0:15], v[48:51], v[104:107], a[0:15]
	ds_read_b128 v[28:31], v98 offset:6144
	ds_read_b128 v[32:35], v98 offset:7168
	ds_read_b128 v[36:39], v98 offset:8192
	ds_read_b128 v[40:43], v98 offset:9216
	ds_read_b128 v[44:47], v98 offset:10240
	ds_read_b128 v[48:51], v98 offset:11264
	s_waitcnt lgkmcnt(6)
	v_mfma_f32_32x32x16_f16 a[80:95], v[4:7], v[108:111], a[80:95]
	v_mfma_f32_32x32x16_f16 a[64:79], v[8:11], v[108:111], a[64:79]
	v_mfma_f32_32x32x16_f16 a[48:63], v[12:15], v[108:111], a[48:63]
	v_mfma_f32_32x32x16_f16 a[32:47], v[16:19], v[108:111], a[32:47]
	v_mfma_f32_32x32x16_f16 a[16:31], v[20:23], v[108:111], a[16:31]
	v_mfma_f32_32x32x16_f16 a[0:15], v[24:27], v[108:111], a[0:15]
	s_waitcnt vmcnt(26)
	ds_write_b128 v81, v[148:151]
	ds_write_b128 v81, v[152:155] offset:1024
	ds_write_b128 v81, v[156:159] offset:2048
	ds_write_b128 v81, v[72:75] offset:3072
	ds_read_b128 v[52:55], v95
	ds_read_b128 v[56:59], v96
	ds_read_b128 v[60:63], v97
	ds_read_b128 v[0:3], v94
	global_load_dwordx4 v[148:151], v64, s[4:5] offset:1408
	global_load_dwordx4 v[152:155], v66, s[4:5] offset:1408
	global_load_dwordx4 v[156:159], v68, s[4:5] offset:1408
	global_load_dwordx4 v[72:75], v70, s[4:5] offset:1408
	s_waitcnt vmcnt(14)
	s_waitcnt lgkmcnt(8)
	s_barrier
	s_add_u32 m0, s46, 0x103c0
	s_add_u32 s40, s40, 0x1800
	s_addc_u32 s41, s41, 0
	global_load_lds_dwordx4 v84, s[40:41]
	s_add_u32 m0, s47, 0x103c0
	s_add_u32 s42, s42, 0x1800
	s_addc_u32 s43, s43, 0
	global_load_lds_dwordx4 v84, s[42:43]
	s_add_u32 m0, s48, 0x103c0
	s_add_u32 s44, s44, 0x1800
	s_addc_u32 s45, s45, 0
	global_load_lds_dwordx4 v84, s[44:45]
	ds_read_b128 v[4:7], v84 offset:0
	ds_read_b128 v[8:11], v84 offset:1024
	ds_read_b128 v[12:15], v84 offset:2048
	ds_read_b128 v[16:19], v84 offset:3072
	ds_read_b128 v[20:23], v84 offset:4096
	ds_read_b128 v[24:27], v84 offset:5120
	v_mfma_f32_32x32x16_f16 a[80:95], v[28:31], v[112:115], a[80:95]
	v_mfma_f32_32x32x16_f16 a[64:79], v[32:35], v[112:115], a[64:79]
	v_mfma_f32_32x32x16_f16 a[48:63], v[36:39], v[112:115], a[48:63]
	v_mfma_f32_32x32x16_f16 a[32:47], v[40:43], v[112:115], a[32:47]
	v_mfma_f32_32x32x16_f16 a[16:31], v[44:47], v[112:115], a[16:31]
	v_mfma_f32_32x32x16_f16 a[0:15], v[48:51], v[112:115], a[0:15]
	s_waitcnt lgkmcnt(6)
	ds_read_b128 v[28:31], v84 offset:6144
	ds_read_b128 v[32:35], v84 offset:7168
	ds_read_b128 v[36:39], v84 offset:8192
	ds_read_b128 v[40:43], v84 offset:9216
	ds_read_b128 v[44:47], v84 offset:10240
	ds_read_b128 v[48:51], v84 offset:11264
	s_waitcnt lgkmcnt(6)
	v_mfma_f32_32x32x16_f16 a[80:95], v[4:7], v[52:55], a[80:95]
	v_mfma_f32_32x32x16_f16 a[64:79], v[8:11], v[52:55], a[64:79]
	v_mfma_f32_32x32x16_f16 a[48:63], v[12:15], v[52:55], a[48:63]
	v_mfma_f32_32x32x16_f16 a[32:47], v[16:19], v[52:55], a[32:47]
	v_mfma_f32_32x32x16_f16 a[16:31], v[20:23], v[52:55], a[16:31]
	v_mfma_f32_32x32x16_f16 a[0:15], v[24:27], v[52:55], a[0:15]
	s_waitcnt vmcnt(10)
	s_waitcnt lgkmcnt(0)
	s_barrier
	s_add_u32 m0, s46, 0x0
	s_add_u32 s40, s40, 0x1800
	s_addc_u32 s41, s41, 0
	global_load_lds_dwordx4 v84, s[40:41]
	s_add_u32 m0, s47, 0x0
	s_add_u32 s42, s42, 0x1800
	s_addc_u32 s43, s43, 0
	global_load_lds_dwordx4 v84, s[42:43]
	s_add_u32 m0, s48, 0x0
	s_add_u32 s44, s44, 0x1800
	s_addc_u32 s45, s45, 0
	global_load_lds_dwordx4 v84, s[44:45]
	ds_read_b128 v[4:7], v84 offset:12288
	ds_read_b128 v[8:11], v84 offset:13312
	ds_read_b128 v[12:15], v84 offset:14336
	ds_read_b128 v[16:19], v84 offset:15360
	ds_read_b128 v[20:23], v84 offset:16384
	ds_read_b128 v[24:27], v84 offset:17408
	v_mfma_f32_32x32x16_f16 a[80:95], v[28:31], v[56:59], a[80:95]
	v_mfma_f32_32x32x16_f16 a[64:79], v[32:35], v[56:59], a[64:79]
	v_mfma_f32_32x32x16_f16 a[48:63], v[36:39], v[56:59], a[48:63]
	v_mfma_f32_32x32x16_f16 a[32:47], v[40:43], v[56:59], a[32:47]
	v_mfma_f32_32x32x16_f16 a[16:31], v[44:47], v[56:59], a[16:31]
	v_mfma_f32_32x32x16_f16 a[0:15], v[48:51], v[56:59], a[0:15]
	ds_read_b128 v[28:31], v84 offset:18432
	ds_read_b128 v[32:35], v84 offset:19456
	ds_read_b128 v[36:39], v84 offset:20480
	ds_read_b128 v[40:43], v84 offset:21504
	ds_read_b128 v[44:47], v84 offset:22528
	ds_read_b128 v[48:51], v84 offset:23552
	s_waitcnt lgkmcnt(6)
	v_mfma_f32_32x32x16_f16 a[80:95], v[4:7], v[60:63], a[80:95]
	v_mfma_f32_32x32x16_f16 a[64:79], v[8:11], v[60:63], a[64:79]
	v_mfma_f32_32x32x16_f16 a[48:63], v[12:15], v[60:63], a[48:63]
	v_mfma_f32_32x32x16_f16 a[32:47], v[16:19], v[60:63], a[32:47]
	v_mfma_f32_32x32x16_f16 a[16:31], v[20:23], v[60:63], a[16:31]
	v_mfma_f32_32x32x16_f16 a[0:15], v[24:27], v[60:63], a[0:15]
	s_waitcnt vmcnt(26)
	ds_write_b128 v81, v[116:119]
	ds_write_b128 v81, v[120:123] offset:1024
	ds_write_b128 v81, v[124:127] offset:2048
	ds_write_b128 v81, v[128:131] offset:3072
	ds_read_b128 v[100:103], v95
	ds_read_b128 v[104:107], v96
	ds_read_b128 v[108:111], v97
	ds_read_b128 v[112:115], v94
	global_load_dwordx4 v[116:119], v64, s[4:5] offset:1440
	global_load_dwordx4 v[120:123], v66, s[4:5] offset:1440
	global_load_dwordx4 v[124:127], v68, s[4:5] offset:1440
	global_load_dwordx4 v[128:131], v70, s[4:5] offset:1440
	s_waitcnt vmcnt(14)
	s_waitcnt lgkmcnt(8)
	s_barrier
	s_add_u32 m0, s46, 0x3000
	s_add_u32 s40, s40, 0x1800
	s_addc_u32 s41, s41, 0
	global_load_lds_dwordx4 v84, s[40:41]
	s_add_u32 m0, s47, 0x3000
	s_add_u32 s42, s42, 0x1800
	s_addc_u32 s43, s43, 0
	global_load_lds_dwordx4 v84, s[42:43]
	s_add_u32 m0, s48, 0x3000
	s_add_u32 s44, s44, 0x1800
	s_addc_u32 s45, s45, 0
	global_load_lds_dwordx4 v84, s[44:45]
	ds_read_b128 v[4:7], v84 offset:54208
	ds_read_b128 v[8:11], v84 offset:55232
	ds_read_b128 v[12:15], v84 offset:56256
	ds_read_b128 v[16:19], v84 offset:57280
	ds_read_b128 v[20:23], v84 offset:58304
	ds_read_b128 v[24:27], v84 offset:59328
	v_mfma_f32_32x32x16_f16 a[80:95], v[28:31], v[0:3], a[80:95]
	v_mfma_f32_32x32x16_f16 a[64:79], v[32:35], v[0:3], a[64:79]
	v_mfma_f32_32x32x16_f16 a[48:63], v[36:39], v[0:3], a[48:63]
	v_mfma_f32_32x32x16_f16 a[32:47], v[40:43], v[0:3], a[32:47]
	v_mfma_f32_32x32x16_f16 a[16:31], v[44:47], v[0:3], a[16:31]
	v_mfma_f32_32x32x16_f16 a[0:15], v[48:51], v[0:3], a[0:15]
	s_waitcnt lgkmcnt(6)
	ds_read_b128 v[28:31], v84 offset:60352
	ds_read_b128 v[32:35], v84 offset:61376
	ds_read_b128 v[36:39], v84 offset:62400
	ds_read_b128 v[40:43], v84 offset:63424
	ds_read_b128 v[44:47], v84 offset:64448
	ds_read_b128 v[48:51], v84 offset:65472
	s_waitcnt lgkmcnt(6)
	v_mfma_f32_32x32x16_f16 a[80:95], v[4:7], v[100:103], a[80:95]
	v_mfma_f32_32x32x16_f16 a[64:79], v[8:11], v[100:103], a[64:79]
	v_mfma_f32_32x32x16_f16 a[48:63], v[12:15], v[100:103], a[48:63]
	v_mfma_f32_32x32x16_f16 a[32:47], v[16:19], v[100:103], a[32:47]
	v_mfma_f32_32x32x16_f16 a[16:31], v[20:23], v[100:103], a[16:31]
	v_mfma_f32_32x32x16_f16 a[0:15], v[24:27], v[100:103], a[0:15]
	s_waitcnt vmcnt(10)
	s_waitcnt lgkmcnt(0)
	s_barrier
	s_add_u32 m0, s46, 0xd3c0
	s_add_u32 s40, s40, 0x1800
	s_addc_u32 s41, s41, 0
	global_load_lds_dwordx4 v84, s[40:41]
	s_add_u32 m0, s47, 0xd3c0
	s_add_u32 s42, s42, 0x1800
	s_addc_u32 s43, s43, 0
	global_load_lds_dwordx4 v84, s[42:43]
	s_add_u32 m0, s48, 0xd3c0
	s_add_u32 s44, s44, 0x1800
	s_addc_u32 s45, s45, 0
	global_load_lds_dwordx4 v84, s[44:45]
	ds_read_b128 v[4:7], v98
	ds_read_b128 v[8:11], v98 offset:1024
	ds_read_b128 v[12:15], v98 offset:2048
	ds_read_b128 v[16:19], v98 offset:3072
	ds_read_b128 v[20:23], v98 offset:4096
	ds_read_b128 v[24:27], v98 offset:5120
	v_mfma_f32_32x32x16_f16 a[80:95], v[28:31], v[104:107], a[80:95]
	v_mfma_f32_32x32x16_f16 a[64:79], v[32:35], v[104:107], a[64:79]
	v_mfma_f32_32x32x16_f16 a[48:63], v[36:39], v[104:107], a[48:63]
	v_mfma_f32_32x32x16_f16 a[32:47], v[40:43], v[104:107], a[32:47]
	v_mfma_f32_32x32x16_f16 a[16:31], v[44:47], v[104:107], a[16:31]
	v_mfma_f32_32x32x16_f16 a[0:15], v[48:51], v[104:107], a[0:15]
	ds_read_b128 v[28:31], v98 offset:6144
	ds_read_b128 v[32:35], v98 offset:7168
	ds_read_b128 v[36:39], v98 offset:8192
	ds_read_b128 v[40:43], v98 offset:9216
	ds_read_b128 v[44:47], v98 offset:10240
	ds_read_b128 v[48:51], v98 offset:11264
	s_waitcnt lgkmcnt(6)
	v_mfma_f32_32x32x16_f16 a[80:95], v[4:7], v[108:111], a[80:95]
	v_mfma_f32_32x32x16_f16 a[64:79], v[8:11], v[108:111], a[64:79]
	v_mfma_f32_32x32x16_f16 a[48:63], v[12:15], v[108:111], a[48:63]
	v_mfma_f32_32x32x16_f16 a[32:47], v[16:19], v[108:111], a[32:47]
	v_mfma_f32_32x32x16_f16 a[16:31], v[20:23], v[108:111], a[16:31]
	v_mfma_f32_32x32x16_f16 a[0:15], v[24:27], v[108:111], a[0:15]
	s_waitcnt vmcnt(26)
	ds_write_b128 v81, v[132:135]
	ds_write_b128 v81, v[136:139] offset:1024
	ds_write_b128 v81, v[140:143] offset:2048
	ds_write_b128 v81, v[144:147] offset:3072
	ds_read_b128 v[52:55], v95
	ds_read_b128 v[56:59], v96
	ds_read_b128 v[60:63], v97
	ds_read_b128 v[0:3], v94
	s_waitcnt vmcnt(10)
	s_waitcnt lgkmcnt(8)
	s_barrier
	s_add_u32 m0, s46, 0x103c0
	s_add_u32 s40, s40, 0x1800
	s_addc_u32 s41, s41, 0
	global_load_lds_dwordx4 v84, s[40:41]
	s_add_u32 m0, s47, 0x103c0
	s_add_u32 s42, s42, 0x1800
	s_addc_u32 s43, s43, 0
	global_load_lds_dwordx4 v84, s[42:43]
	s_add_u32 m0, s48, 0x103c0
	s_add_u32 s44, s44, 0x1800
	s_addc_u32 s45, s45, 0
	global_load_lds_dwordx4 v84, s[44:45]
	ds_read_b128 v[4:7], v84 offset:0
	ds_read_b128 v[8:11], v84 offset:1024
	ds_read_b128 v[12:15], v84 offset:2048
	ds_read_b128 v[16:19], v84 offset:3072
	ds_read_b128 v[20:23], v84 offset:4096
	ds_read_b128 v[24:27], v84 offset:5120
	v_mfma_f32_32x32x16_f16 a[80:95], v[28:31], v[112:115], a[80:95]
	v_mfma_f32_32x32x16_f16 a[64:79], v[32:35], v[112:115], a[64:79]
	v_mfma_f32_32x32x16_f16 a[48:63], v[36:39], v[112:115], a[48:63]
	v_mfma_f32_32x32x16_f16 a[32:47], v[40:43], v[112:115], a[32:47]
	v_mfma_f32_32x32x16_f16 a[16:31], v[44:47], v[112:115], a[16:31]
	v_mfma_f32_32x32x16_f16 a[0:15], v[48:51], v[112:115], a[0:15]
	s_waitcnt lgkmcnt(6)
	ds_read_b128 v[28:31], v84 offset:6144
	ds_read_b128 v[32:35], v84 offset:7168
	ds_read_b128 v[36:39], v84 offset:8192
	ds_read_b128 v[40:43], v84 offset:9216
	ds_read_b128 v[44:47], v84 offset:10240
	ds_read_b128 v[48:51], v84 offset:11264
	s_waitcnt lgkmcnt(6)
	v_mfma_f32_32x32x16_f16 a[80:95], v[4:7], v[52:55], a[80:95]
	v_mfma_f32_32x32x16_f16 a[64:79], v[8:11], v[52:55], a[64:79]
	v_mfma_f32_32x32x16_f16 a[48:63], v[12:15], v[52:55], a[48:63]
	v_mfma_f32_32x32x16_f16 a[32:47], v[16:19], v[52:55], a[32:47]
	v_mfma_f32_32x32x16_f16 a[16:31], v[20:23], v[52:55], a[16:31]
	v_mfma_f32_32x32x16_f16 a[0:15], v[24:27], v[52:55], a[0:15]
	s_waitcnt vmcnt(6)
	s_waitcnt lgkmcnt(0)
	s_barrier
	s_add_u32 m0, s46, 0x0
	s_add_u32 s40, s40, 0x1800
	s_addc_u32 s41, s41, 0
	global_load_lds_dwordx4 v84, s[40:41]
	s_add_u32 m0, s47, 0x0
	s_add_u32 s42, s42, s49
	s_addc_u32 s43, s43, 0
	global_load_lds_dwordx4 v84, s[42:43]
	s_add_u32 m0, s48, 0x0
	s_add_u32 s44, s44, 0xc00
	s_addc_u32 s45, s45, 0
	global_load_lds_dwordx4 v84, s[44:45]
	ds_read_b128 v[4:7], v84 offset:12288
	ds_read_b128 v[8:11], v84 offset:13312
	ds_read_b128 v[12:15], v84 offset:14336
	ds_read_b128 v[16:19], v84 offset:15360
	ds_read_b128 v[20:23], v84 offset:16384
	ds_read_b128 v[24:27], v84 offset:17408
	v_mfma_f32_32x32x16_f16 a[80:95], v[28:31], v[56:59], a[80:95]
	v_mfma_f32_32x32x16_f16 a[64:79], v[32:35], v[56:59], a[64:79]
	v_mfma_f32_32x32x16_f16 a[48:63], v[36:39], v[56:59], a[48:63]
	v_mfma_f32_32x32x16_f16 a[32:47], v[40:43], v[56:59], a[32:47]
	v_mfma_f32_32x32x16_f16 a[16:31], v[44:47], v[56:59], a[16:31]
	v_mfma_f32_32x32x16_f16 a[0:15], v[48:51], v[56:59], a[0:15]
	ds_read_b128 v[28:31], v84 offset:18432
	ds_read_b128 v[32:35], v84 offset:19456
	ds_read_b128 v[36:39], v84 offset:20480
	ds_read_b128 v[40:43], v84 offset:21504
	ds_read_b128 v[44:47], v84 offset:22528
	ds_read_b128 v[48:51], v84 offset:23552
	s_waitcnt lgkmcnt(6)
	v_mfma_f32_32x32x16_f16 a[80:95], v[4:7], v[60:63], a[80:95]
	v_mfma_f32_32x32x16_f16 a[64:79], v[8:11], v[60:63], a[64:79]
	v_mfma_f32_32x32x16_f16 a[48:63], v[12:15], v[60:63], a[48:63]
	v_mfma_f32_32x32x16_f16 a[32:47], v[16:19], v[60:63], a[32:47]
	v_mfma_f32_32x32x16_f16 a[16:31], v[20:23], v[60:63], a[16:31]
	v_mfma_f32_32x32x16_f16 a[0:15], v[24:27], v[60:63], a[0:15]
	s_waitcnt vmcnt(22)
	ds_write_b128 v81, v[148:151]
	ds_write_b128 v81, v[152:155] offset:1024
	ds_write_b128 v81, v[156:159] offset:2048
	ds_write_b128 v81, v[72:75] offset:3072
	ds_read_b128 v[100:103], v95
	ds_read_b128 v[104:107], v96
	ds_read_b128 v[108:111], v97
	ds_read_b128 v[112:115], v94
	s_waitcnt vmcnt(6)
	s_waitcnt lgkmcnt(8)
	s_barrier
	ds_read_b128 v[4:7], v84 offset:54208
	ds_read_b128 v[8:11], v84 offset:55232
	ds_read_b128 v[12:15], v84 offset:56256
	ds_read_b128 v[16:19], v84 offset:57280
	ds_read_b128 v[20:23], v84 offset:58304
	ds_read_b128 v[24:27], v84 offset:59328
	v_mfma_f32_32x32x16_f16 a[80:95], v[28:31], v[0:3], a[80:95]
	v_mfma_f32_32x32x16_f16 a[64:79], v[32:35], v[0:3], a[64:79]
	v_mfma_f32_32x32x16_f16 a[48:63], v[36:39], v[0:3], a[48:63]
	v_mfma_f32_32x32x16_f16 a[32:47], v[40:43], v[0:3], a[32:47]
	v_mfma_f32_32x32x16_f16 a[16:31], v[44:47], v[0:3], a[16:31]
	v_mfma_f32_32x32x16_f16 a[0:15], v[48:51], v[0:3], a[0:15]
	s_waitcnt lgkmcnt(6)
	ds_read_b128 v[28:31], v84 offset:60352
	ds_read_b128 v[32:35], v84 offset:61376
	ds_read_b128 v[36:39], v84 offset:62400
	ds_read_b128 v[40:43], v84 offset:63424
	ds_read_b128 v[44:47], v84 offset:64448
	ds_read_b128 v[48:51], v84 offset:65472
	s_waitcnt lgkmcnt(6)
	v_mfma_f32_32x32x16_f16 a[80:95], v[4:7], v[100:103], a[80:95]
	v_mfma_f32_32x32x16_f16 a[64:79], v[8:11], v[100:103], a[64:79]
	v_mfma_f32_32x32x16_f16 a[48:63], v[12:15], v[100:103], a[48:63]
	v_mfma_f32_32x32x16_f16 a[32:47], v[16:19], v[100:103], a[32:47]
	v_mfma_f32_32x32x16_f16 a[16:31], v[20:23], v[100:103], a[16:31]
	v_mfma_f32_32x32x16_f16 a[0:15], v[24:27], v[100:103], a[0:15]
	s_waitcnt vmcnt(3)
	s_waitcnt lgkmcnt(0)
	s_barrier
	ds_read_b128 v[4:7], v98
	ds_read_b128 v[8:11], v98 offset:1024
	ds_read_b128 v[12:15], v98 offset:2048
	ds_read_b128 v[16:19], v98 offset:3072
	ds_read_b128 v[20:23], v98 offset:4096
	ds_read_b128 v[24:27], v98 offset:5120
	v_mfma_f32_32x32x16_f16 a[80:95], v[28:31], v[104:107], a[80:95]
	v_mfma_f32_32x32x16_f16 a[64:79], v[32:35], v[104:107], a[64:79]
	v_mfma_f32_32x32x16_f16 a[48:63], v[36:39], v[104:107], a[48:63]
	v_mfma_f32_32x32x16_f16 a[32:47], v[40:43], v[104:107], a[32:47]
	v_mfma_f32_32x32x16_f16 a[16:31], v[44:47], v[104:107], a[16:31]
	v_mfma_f32_32x32x16_f16 a[0:15], v[48:51], v[104:107], a[0:15]
	ds_read_b128 v[28:31], v98 offset:6144
	ds_read_b128 v[32:35], v98 offset:7168
	ds_read_b128 v[36:39], v98 offset:8192
	ds_read_b128 v[40:43], v98 offset:9216
	ds_read_b128 v[44:47], v98 offset:10240
	ds_read_b128 v[48:51], v98 offset:11264
	s_waitcnt lgkmcnt(6)
	v_mfma_f32_32x32x16_f16 a[80:95], v[4:7], v[108:111], a[80:95]
	v_mfma_f32_32x32x16_f16 a[64:79], v[8:11], v[108:111], a[64:79]
	v_mfma_f32_32x32x16_f16 a[48:63], v[12:15], v[108:111], a[48:63]
	v_mfma_f32_32x32x16_f16 a[32:47], v[16:19], v[108:111], a[32:47]
	v_mfma_f32_32x32x16_f16 a[16:31], v[20:23], v[108:111], a[16:31]
	v_mfma_f32_32x32x16_f16 a[0:15], v[24:27], v[108:111], a[0:15]
	s_waitcnt vmcnt(12)
	ds_write_b128 v81, v[116:119]
	ds_write_b128 v81, v[120:123] offset:1024
	ds_write_b128 v81, v[124:127] offset:2048
	ds_write_b128 v81, v[128:131] offset:3072
	ds_read_b128 v[0:3], v94
	s_waitcnt vmcnt(0)
	s_waitcnt lgkmcnt(5)
	s_barrier
	ds_read_b128 v[4:7], v84 offset:0
	ds_read_b128 v[8:11], v84 offset:1024
	ds_read_b128 v[12:15], v84 offset:2048
	ds_read_b128 v[16:19], v84 offset:3072
	ds_read_b128 v[20:23], v84 offset:4096
	ds_read_b128 v[24:27], v84 offset:5120
	v_mfma_f32_32x32x16_f16 a[80:95], v[28:31], v[112:115], a[80:95]
	v_mfma_f32_32x32x16_f16 a[64:79], v[32:35], v[112:115], a[64:79]
	v_mfma_f32_32x32x16_f16 a[48:63], v[36:39], v[112:115], a[48:63]
	v_mfma_f32_32x32x16_f16 a[32:47], v[40:43], v[112:115], a[32:47]
	v_mfma_f32_32x32x16_f16 a[16:31], v[44:47], v[112:115], a[16:31]
	v_mfma_f32_32x32x16_f16 a[0:15], v[48:51], v[112:115], a[0:15]
	s_waitcnt lgkmcnt(0)
	v_mfma_f32_32x32x16_f16 a[80:95], v[4:7], v[0:3], a[80:95]
	v_mfma_f32_32x32x16_f16 a[16:31], v[20:23], v[0:3], a[16:31]
	v_lshlrev_b32_e32 v22, 4, v85
	v_mfma_f32_32x32x16_f16 a[64:79], v[8:11], v[0:3], a[64:79]
	v_mfma_f32_32x32x16_f16 a[48:63], v[12:15], v[0:3], a[48:63]
	s_nop 7
	v_accvgpr_read_b32 v13, a88
	v_mfma_f32_32x32x16_f16 a[32:47], v[16:19], v[0:3], a[32:47]
	v_accvgpr_read_b32 v17, a92
	v_mfma_f32_32x32x16_f16 a[0:15], v[24:27], v[0:3], a[0:15]
	ds_read_b128 v[2:5], v22 offset:53248
	ds_read_b128 v[6:9], v22 offset:53280
	v_accvgpr_read_b32 v1, a80
	v_lshlrev_b32_e32 v0, 4, v92
	s_waitcnt lgkmcnt(1)
	v_add_f32_e32 v1, v1, v2
	v_accvgpr_read_b32 v2, a81
	v_add_f32_e32 v2, v3, v2
	v_max_f32_e32 v10, 0, v2
	v_accvgpr_read_b32 v2, a82
	v_add_f32_e32 v2, v4, v2
	v_max_f32_e32 v11, 0, v2
	v_accvgpr_read_b32 v2, a83
	v_add_f32_e32 v2, v5, v2
	v_max_f32_e32 v12, 0, v2
	v_accvgpr_read_b32 v2, a84
	s_waitcnt lgkmcnt(0)
	v_add_f32_e32 v2, v2, v6
	v_max_f32_e32 v6, 0, v2
	v_accvgpr_read_b32 v2, a85
	v_add_f32_e32 v2, v7, v2
	v_max_f32_e32 v7, 0, v2
	v_accvgpr_read_b32 v2, a86
	v_add_f32_e32 v2, v8, v2
	v_max_f32_e32 v8, 0, v2
	v_accvgpr_read_b32 v2, a87
	v_add_f32_e32 v2, v9, v2
	v_max_f32_e32 v9, 0, v2
	ds_read_b128 v[2:5], v22 offset:53312
	v_max_f32_e32 v1, 0, v1
	s_waitcnt lgkmcnt(0)
	v_add_f32_e32 v2, v13, v2
	v_max_f32_e32 v13, 0, v2
	v_accvgpr_read_b32 v2, a89
	v_add_f32_e32 v2, v3, v2
	v_max_f32_e32 v14, 0, v2
	v_accvgpr_read_b32 v2, a90
	v_add_f32_e32 v2, v4, v2
	v_max_f32_e32 v15, 0, v2
	v_accvgpr_read_b32 v2, a91
	v_add_f32_e32 v2, v5, v2
	v_max_f32_e32 v16, 0, v2
	ds_read_b128 v[2:5], v22 offset:53344
	s_waitcnt lgkmcnt(0)
	v_add_f32_e32 v2, v17, v2
	v_max_f32_e32 v17, 0, v2
	v_accvgpr_read_b32 v2, a93
	v_add_f32_e32 v2, v3, v2
	v_max_f32_e32 v18, 0, v2
	v_accvgpr_read_b32 v2, a94
	v_add_f32_e32 v2, v4, v2
	v_max_f32_e32 v19, 0, v2
	v_accvgpr_read_b32 v2, a95
	v_add_f32_e32 v2, v5, v2
	v_cvt_pk_f16_f32 v5, v8, v9
	v_cvt_pk_f16_f32 v4, v6, v7
	ds_read_b128 v[6:9], v0 offset:40960
	v_max_f32_e32 v20, 0, v2
	v_cvt_pk_f16_f32 v3, v11, v12
	v_cvt_pk_f16_f32 v2, v1, v10
	v_accvgpr_read_b32 v1, a64
	s_waitcnt lgkmcnt(0)
	v_mfma_f32_32x32x16_f16 a[80:95], v[6:9], v[2:5], 0
	ds_read_b128 v[6:9], v0 offset:41984
	v_cvt_pk_f16_f32 v5, v19, v20
	v_cvt_pk_f16_f32 v4, v17, v18
	v_cvt_pk_f16_f32 v3, v15, v16
	v_cvt_pk_f16_f32 v2, v13, v14
	v_accvgpr_read_b32 v13, a72
	v_accvgpr_read_b32 v17, a76
	s_waitcnt lgkmcnt(0)
	v_mfma_f32_32x32x16_f16 a[80:95], v[6:9], v[2:5], a[80:95]
	ds_read_b128 v[2:5], v22 offset:53376
	v_accvgpr_read_b32 v9, a68
	s_waitcnt lgkmcnt(0)
	v_add_f32_e32 v1, v1, v2
	v_accvgpr_read_b32 v2, a65
	v_add_f32_e32 v2, v3, v2
	v_max_f32_e32 v6, 0, v2
	v_accvgpr_read_b32 v2, a66
	v_add_f32_e32 v2, v4, v2
	v_max_f32_e32 v7, 0, v2
	v_accvgpr_read_b32 v2, a67
	v_add_f32_e32 v2, v5, v2
	v_max_f32_e32 v8, 0, v2
	ds_read_b128 v[2:5], v22 offset:53408
	v_max_f32_e32 v1, 0, v1
	s_waitcnt lgkmcnt(0)
	v_add_f32_e32 v2, v9, v2
	v_max_f32_e32 v9, 0, v2
	v_accvgpr_read_b32 v2, a69
	v_add_f32_e32 v2, v3, v2
	v_max_f32_e32 v10, 0, v2
	v_accvgpr_read_b32 v2, a70
	v_add_f32_e32 v2, v4, v2
	v_max_f32_e32 v11, 0, v2
	v_accvgpr_read_b32 v2, a71
	v_add_f32_e32 v2, v5, v2
	v_max_f32_e32 v12, 0, v2
	ds_read_b128 v[2:5], v22 offset:53440
	s_waitcnt lgkmcnt(0)
	v_add_f32_e32 v2, v13, v2
	v_max_f32_e32 v13, 0, v2
	v_accvgpr_read_b32 v2, a73
	v_add_f32_e32 v2, v3, v2
	v_max_f32_e32 v14, 0, v2
	v_accvgpr_read_b32 v2, a74
	v_add_f32_e32 v2, v4, v2
	v_max_f32_e32 v15, 0, v2
	v_accvgpr_read_b32 v2, a75
	v_add_f32_e32 v2, v5, v2
	v_max_f32_e32 v16, 0, v2
	ds_read_b128 v[2:5], v22 offset:53472
	s_waitcnt lgkmcnt(0)
	v_add_f32_e32 v2, v17, v2
	v_max_f32_e32 v17, 0, v2
	v_accvgpr_read_b32 v2, a77
	v_add_f32_e32 v2, v3, v2
	v_max_f32_e32 v18, 0, v2
	v_accvgpr_read_b32 v2, a78
	v_add_f32_e32 v2, v4, v2
	v_max_f32_e32 v19, 0, v2
	v_accvgpr_read_b32 v2, a79
	v_add_f32_e32 v2, v5, v2
	v_max_f32_e32 v20, 0, v2
	v_cvt_pk_f16_f32 v4, v9, v10
	v_cvt_pk_f16_f32 v3, v7, v8
	v_cvt_pk_f16_f32 v2, v1, v6
	ds_read_b128 v[6:9], v0 offset:43008
	v_cvt_pk_f16_f32 v5, v11, v12
	v_accvgpr_read_b32 v1, a48
	s_waitcnt lgkmcnt(0)
	v_mfma_f32_32x32x16_f16 a[80:95], v[6:9], v[2:5], a[80:95]
	ds_read_b128 v[6:9], v0 offset:44032
	v_cvt_pk_f16_f32 v5, v19, v20
	v_cvt_pk_f16_f32 v4, v17, v18
	v_cvt_pk_f16_f32 v3, v15, v16
	v_cvt_pk_f16_f32 v2, v13, v14
	v_accvgpr_read_b32 v13, a56
	v_accvgpr_read_b32 v17, a60
	s_waitcnt lgkmcnt(0)
	v_mfma_f32_32x32x16_f16 a[80:95], v[6:9], v[2:5], a[80:95]
	ds_read_b128 v[2:5], v22 offset:53504
	v_accvgpr_read_b32 v9, a52
	s_waitcnt lgkmcnt(0)
	v_add_f32_e32 v1, v1, v2
	v_accvgpr_read_b32 v2, a49
	v_add_f32_e32 v2, v3, v2
	v_max_f32_e32 v6, 0, v2
	v_accvgpr_read_b32 v2, a50
	v_add_f32_e32 v2, v4, v2
	v_max_f32_e32 v7, 0, v2
	v_accvgpr_read_b32 v2, a51
	v_add_f32_e32 v2, v5, v2
	v_max_f32_e32 v8, 0, v2
	ds_read_b128 v[2:5], v22 offset:53536
	v_max_f32_e32 v1, 0, v1
	s_waitcnt lgkmcnt(0)
	v_add_f32_e32 v2, v9, v2
	v_max_f32_e32 v9, 0, v2
	v_accvgpr_read_b32 v2, a53
	v_add_f32_e32 v2, v3, v2
	v_max_f32_e32 v10, 0, v2
	v_accvgpr_read_b32 v2, a54
	v_add_f32_e32 v2, v4, v2
	v_max_f32_e32 v11, 0, v2
	v_accvgpr_read_b32 v2, a55
	v_add_f32_e32 v2, v5, v2
	v_max_f32_e32 v12, 0, v2
	ds_read_b128 v[2:5], v22 offset:53568
	s_waitcnt lgkmcnt(0)
	v_add_f32_e32 v2, v13, v2
	v_max_f32_e32 v13, 0, v2
	v_accvgpr_read_b32 v2, a57
	v_add_f32_e32 v2, v3, v2
	v_max_f32_e32 v14, 0, v2
	v_accvgpr_read_b32 v2, a58
	v_add_f32_e32 v2, v4, v2
	v_max_f32_e32 v15, 0, v2
	v_accvgpr_read_b32 v2, a59
	v_add_f32_e32 v2, v5, v2
	v_max_f32_e32 v16, 0, v2
	ds_read_b128 v[2:5], v22 offset:53600
	s_waitcnt lgkmcnt(0)
	v_add_f32_e32 v2, v17, v2
	v_max_f32_e32 v17, 0, v2
	v_accvgpr_read_b32 v2, a61
	v_add_f32_e32 v2, v3, v2
	v_max_f32_e32 v18, 0, v2
	v_accvgpr_read_b32 v2, a62
	v_add_f32_e32 v2, v4, v2
	v_max_f32_e32 v19, 0, v2
	v_accvgpr_read_b32 v2, a63
	v_add_f32_e32 v2, v5, v2
	v_max_f32_e32 v20, 0, v2
	v_cvt_pk_f16_f32 v4, v9, v10
	v_cvt_pk_f16_f32 v3, v7, v8
	v_cvt_pk_f16_f32 v2, v1, v6
	ds_read_b128 v[6:9], v0 offset:45056
	v_cvt_pk_f16_f32 v5, v11, v12
	v_accvgpr_read_b32 v1, a32
	s_waitcnt lgkmcnt(0)
	v_mfma_f32_32x32x16_f16 a[80:95], v[6:9], v[2:5], a[80:95]
	ds_read_b128 v[6:9], v0 offset:46080
	v_cvt_pk_f16_f32 v5, v19, v20
	v_cvt_pk_f16_f32 v4, v17, v18
	v_cvt_pk_f16_f32 v3, v15, v16
	v_cvt_pk_f16_f32 v2, v13, v14
	v_accvgpr_read_b32 v13, a40
	v_accvgpr_read_b32 v17, a44
	s_waitcnt lgkmcnt(0)
	v_mfma_f32_32x32x16_f16 a[80:95], v[6:9], v[2:5], a[80:95]
	ds_read_b128 v[2:5], v22 offset:53632
	v_accvgpr_read_b32 v9, a36
	s_waitcnt lgkmcnt(0)
	v_add_f32_e32 v1, v1, v2
	v_accvgpr_read_b32 v2, a33
	v_add_f32_e32 v2, v3, v2
	v_max_f32_e32 v6, 0, v2
	v_accvgpr_read_b32 v2, a34
	v_add_f32_e32 v2, v4, v2
	v_max_f32_e32 v7, 0, v2
	v_accvgpr_read_b32 v2, a35
	v_add_f32_e32 v2, v5, v2
	v_max_f32_e32 v8, 0, v2
	ds_read_b128 v[2:5], v22 offset:53664
	v_max_f32_e32 v1, 0, v1
	s_waitcnt lgkmcnt(0)
	v_add_f32_e32 v2, v9, v2
	v_max_f32_e32 v9, 0, v2
	v_accvgpr_read_b32 v2, a37
	v_add_f32_e32 v2, v3, v2
	v_max_f32_e32 v10, 0, v2
	v_accvgpr_read_b32 v2, a38
	v_add_f32_e32 v2, v4, v2
	v_max_f32_e32 v11, 0, v2
	v_accvgpr_read_b32 v2, a39
	v_add_f32_e32 v2, v5, v2
	v_max_f32_e32 v12, 0, v2
	ds_read_b128 v[2:5], v22 offset:53696
	s_waitcnt lgkmcnt(0)
	v_add_f32_e32 v2, v13, v2
	v_max_f32_e32 v13, 0, v2
	v_accvgpr_read_b32 v2, a41
	v_add_f32_e32 v2, v3, v2
	v_max_f32_e32 v14, 0, v2
	v_accvgpr_read_b32 v2, a42
	v_add_f32_e32 v2, v4, v2
	v_max_f32_e32 v15, 0, v2
	v_accvgpr_read_b32 v2, a43
	v_add_f32_e32 v2, v5, v2
	v_max_f32_e32 v16, 0, v2
	ds_read_b128 v[2:5], v22 offset:53728
	s_waitcnt lgkmcnt(0)
	v_add_f32_e32 v2, v17, v2
	v_max_f32_e32 v17, 0, v2
	v_accvgpr_read_b32 v2, a45
	v_add_f32_e32 v2, v3, v2
	v_max_f32_e32 v18, 0, v2
	v_accvgpr_read_b32 v2, a46
	v_add_f32_e32 v2, v4, v2
	v_max_f32_e32 v19, 0, v2
	v_accvgpr_read_b32 v2, a47
	v_add_f32_e32 v2, v5, v2
	v_max_f32_e32 v20, 0, v2
	v_cvt_pk_f16_f32 v4, v9, v10
	v_cvt_pk_f16_f32 v3, v7, v8
	v_cvt_pk_f16_f32 v2, v1, v6
	ds_read_b128 v[6:9], v0 offset:47104
	v_cvt_pk_f16_f32 v5, v11, v12
	v_accvgpr_read_b32 v1, a16
	s_waitcnt lgkmcnt(0)
	v_mfma_f32_32x32x16_f16 a[32:47], v[6:9], v[2:5], 0
	ds_read_b128 v[6:9], v0 offset:48128
	v_cvt_pk_f16_f32 v5, v19, v20
	v_cvt_pk_f16_f32 v4, v17, v18
	v_cvt_pk_f16_f32 v3, v15, v16
	v_cvt_pk_f16_f32 v2, v13, v14
	v_accvgpr_read_b32 v13, a24
	v_accvgpr_read_b32 v17, a28
	s_waitcnt lgkmcnt(0)
	v_mfma_f32_32x32x16_f16 a[32:47], v[6:9], v[2:5], a[32:47]
	ds_read_b128 v[2:5], v22 offset:53760
	v_accvgpr_read_b32 v9, a20
	s_waitcnt lgkmcnt(0)
	v_add_f32_e32 v1, v1, v2
	v_accvgpr_read_b32 v2, a17
	v_add_f32_e32 v2, v3, v2
	v_max_f32_e32 v6, 0, v2
	v_accvgpr_read_b32 v2, a18
	v_add_f32_e32 v2, v4, v2
	v_max_f32_e32 v7, 0, v2
	v_accvgpr_read_b32 v2, a19
	v_add_f32_e32 v2, v5, v2
	v_max_f32_e32 v8, 0, v2
	ds_read_b128 v[2:5], v22 offset:53792
	v_max_f32_e32 v1, 0, v1
	s_waitcnt lgkmcnt(0)
	v_add_f32_e32 v2, v9, v2
	v_max_f32_e32 v9, 0, v2
	v_accvgpr_read_b32 v2, a21
	v_add_f32_e32 v2, v3, v2
	v_max_f32_e32 v10, 0, v2
	v_accvgpr_read_b32 v2, a22
	v_add_f32_e32 v2, v4, v2
	v_max_f32_e32 v11, 0, v2
	v_accvgpr_read_b32 v2, a23
	v_add_f32_e32 v2, v5, v2
	v_max_f32_e32 v12, 0, v2
	ds_read_b128 v[2:5], v22 offset:53824
	s_waitcnt lgkmcnt(0)
	v_add_f32_e32 v2, v13, v2
	v_max_f32_e32 v13, 0, v2
	v_accvgpr_read_b32 v2, a25
	v_add_f32_e32 v2, v3, v2
	v_max_f32_e32 v14, 0, v2
	v_accvgpr_read_b32 v2, a26
	v_add_f32_e32 v2, v4, v2
	v_max_f32_e32 v15, 0, v2
	v_accvgpr_read_b32 v2, a27
	v_add_f32_e32 v2, v5, v2
	v_max_f32_e32 v16, 0, v2
	ds_read_b128 v[2:5], v22 offset:53856
	s_waitcnt lgkmcnt(0)
	v_add_f32_e32 v2, v17, v2
	v_max_f32_e32 v17, 0, v2
	v_accvgpr_read_b32 v2, a29
	v_add_f32_e32 v2, v3, v2
	v_max_f32_e32 v18, 0, v2
	v_accvgpr_read_b32 v2, a30
	v_add_f32_e32 v2, v4, v2
	v_max_f32_e32 v19, 0, v2
	v_accvgpr_read_b32 v2, a31
	v_add_f32_e32 v2, v5, v2
	v_max_f32_e32 v20, 0, v2
	v_cvt_pk_f16_f32 v4, v9, v10
	v_cvt_pk_f16_f32 v3, v7, v8
	v_cvt_pk_f16_f32 v2, v1, v6
	ds_read_b128 v[6:9], v0 offset:49152
	v_cvt_pk_f16_f32 v5, v11, v12
	v_accvgpr_read_b32 v1, a0
	s_waitcnt lgkmcnt(0)
	v_mfma_f32_32x32x16_f16 a[32:47], v[6:9], v[2:5], a[32:47]
	ds_read_b128 v[6:9], v0 offset:50176
	v_cvt_pk_f16_f32 v5, v19, v20
	v_cvt_pk_f16_f32 v4, v17, v18
	v_cvt_pk_f16_f32 v3, v15, v16
	v_cvt_pk_f16_f32 v2, v13, v14
	v_accvgpr_read_b32 v13, a8
	v_accvgpr_read_b32 v17, a12
	s_waitcnt lgkmcnt(0)
	v_mfma_f32_32x32x16_f16 a[32:47], v[6:9], v[2:5], a[32:47]
	ds_read_b128 v[2:5], v22 offset:53888
	v_accvgpr_read_b32 v9, a4
	s_waitcnt lgkmcnt(0)
	v_add_f32_e32 v1, v1, v2
	v_accvgpr_read_b32 v2, a1
	v_add_f32_e32 v2, v3, v2
	v_max_f32_e32 v6, 0, v2
	v_accvgpr_read_b32 v2, a2
	v_add_f32_e32 v2, v4, v2
	v_max_f32_e32 v7, 0, v2
	v_accvgpr_read_b32 v2, a3
	v_add_f32_e32 v2, v5, v2
	v_max_f32_e32 v8, 0, v2
	ds_read_b128 v[2:5], v22 offset:53920
	v_max_f32_e32 v1, 0, v1
	s_waitcnt lgkmcnt(0)
	v_add_f32_e32 v2, v9, v2
	v_max_f32_e32 v9, 0, v2
	v_accvgpr_read_b32 v2, a5
	v_add_f32_e32 v2, v3, v2
	v_max_f32_e32 v10, 0, v2
	v_accvgpr_read_b32 v2, a6
	v_add_f32_e32 v2, v4, v2
	v_max_f32_e32 v11, 0, v2
	v_accvgpr_read_b32 v2, a7
	v_add_f32_e32 v2, v5, v2
	v_max_f32_e32 v12, 0, v2
	ds_read_b128 v[2:5], v22 offset:53952
	s_waitcnt lgkmcnt(0)
	v_add_f32_e32 v2, v13, v2
	v_max_f32_e32 v13, 0, v2
	v_accvgpr_read_b32 v2, a9
	v_add_f32_e32 v2, v3, v2
	v_max_f32_e32 v14, 0, v2
	v_accvgpr_read_b32 v2, a10
	v_add_f32_e32 v2, v4, v2
	v_max_f32_e32 v15, 0, v2
	v_accvgpr_read_b32 v2, a11
	v_add_f32_e32 v2, v5, v2
	v_max_f32_e32 v16, 0, v2
	ds_read_b128 v[2:5], v22 offset:53984
	s_waitcnt lgkmcnt(0)
	v_add_f32_e32 v2, v17, v2
	v_max_f32_e32 v17, 0, v2
	v_accvgpr_read_b32 v2, a13
	v_add_f32_e32 v2, v3, v2
	v_max_f32_e32 v18, 0, v2
	v_accvgpr_read_b32 v2, a14
	v_add_f32_e32 v2, v4, v2
	v_max_f32_e32 v19, 0, v2
	v_accvgpr_read_b32 v2, a15
	v_add_f32_e32 v2, v5, v2
	v_max_f32_e32 v20, 0, v2
	v_cvt_pk_f16_f32 v4, v9, v10
	v_cvt_pk_f16_f32 v3, v7, v8
	v_cvt_pk_f16_f32 v2, v1, v6
	ds_read_b128 v[6:9], v0 offset:51200
	v_cvt_pk_f16_f32 v5, v11, v12
	s_waitcnt lgkmcnt(0)
	s_nop 0
	v_mfma_f32_32x32x16_f16 a[32:47], v[6:9], v[2:5], a[32:47]
	ds_read_b128 v[6:9], v0 offset:52224
	v_cvt_pk_f16_f32 v5, v19, v20
	v_cvt_pk_f16_f32 v4, v17, v18
	v_cvt_pk_f16_f32 v3, v15, v16
	v_cvt_pk_f16_f32 v2, v13, v14
	s_waitcnt lgkmcnt(0)
	s_nop 0
	v_mfma_f32_32x32x16_f16 a[32:47], v[6:9], v[2:5], a[32:47]
	s_and_saveexec_b64 s[2:3], s[0:1]
	s_cbranch_execz .LBB3_39
	v_accvgpr_read_b32 v0, a80
	v_accvgpr_read_b32 v6, a86
	v_accvgpr_read_b32 v7, a87
	v_accvgpr_read_b32 v8, a88
	v_accvgpr_read_b32 v9, a89
	v_accvgpr_read_b32 v10, a90
	v_accvgpr_read_b32 v11, a91
	v_accvgpr_read_b32 v12, a92
	v_accvgpr_read_b32 v13, a93
	v_accvgpr_read_b32 v14, a94
	v_accvgpr_read_b32 v15, a95
	v_accvgpr_read_b32 v6, a32
	v_accvgpr_read_b32 v14, a40
	v_accvgpr_read_b32 v15, a41
	v_accvgpr_read_b32 v16, a42
	v_accvgpr_read_b32 v17, a43
	v_accvgpr_read_b32 v18, a44
	v_accvgpr_read_b32 v19, a45
	v_accvgpr_read_b32 v20, a46
	v_accvgpr_read_b32 v21, a47
	ds_read_b128 v[14:17], v22 offset:54016
	ds_read_b128 v[18:21], v22 offset:54080
	v_accvgpr_read_b32 v12, a38
	v_accvgpr_read_b32 v13, a39
	v_lshlrev_b32_e32 v24, 2, v85
	v_accvgpr_read_b32 v1, a81
	v_accvgpr_read_b32 v7, a33
	v_mad_i64_i32 v[12:13], s[0:1], v80, 40, s[18:19]
	v_ashrrev_i32_e32 v25, 31, v24
	v_accvgpr_read_b32 v3, a83
	v_accvgpr_read_b32 v9, a35
	v_lshl_add_u64 v[22:23], v[24:25], 2, v[12:13]
	v_mov_b32_e32 v25, v1
	s_waitcnt lgkmcnt(1)
	v_mov_b32_e32 v27, v15
	v_mov_b32_e32 v1, v7
	s_waitcnt lgkmcnt(0)
	v_mov_b32_e32 v15, v19
	v_accvgpr_read_b32 v2, a82
	v_accvgpr_read_b32 v8, a34
	v_pk_add_f32 v[0:1], v[0:1], v[14:15]
	v_mov_b32_e32 v7, v3
	v_mov_b32_e32 v15, v17
	v_mov_b32_e32 v3, v9
	v_mov_b32_e32 v17, v21
	v_mov_b32_e32 v24, v6
	v_mov_b32_e32 v26, v18
	v_mov_b32_e32 v6, v8
	v_mov_b32_e32 v14, v20
	v_pk_add_f32 v[2:3], v[2:3], v[16:17]
	v_pk_add_f32 v[24:25], v[24:25], v[26:27]
	s_waitcnt vmcnt(0)
	v_pk_mul_f32 v[0:1], v[82:83], v[0:1]
	v_pk_add_f32 v[6:7], v[6:7], v[14:15]
	v_pk_mul_f32 v[2:3], v[82:83], v[2:3]
	v_accvgpr_read_b32 v4, a84
	v_accvgpr_read_b32 v5, a85
	v_accvgpr_read_b32 v10, a36
	v_accvgpr_read_b32 v11, a37
	v_pk_fma_f32 v[0:1], v[82:83], v[24:25], v[0:1] op_sel:[1,0,0] op_sel_hi:[0,1,1]
	v_pk_fma_f32 v[2:3], v[82:83], v[6:7], v[2:3] op_sel:[1,0,0] op_sel_hi:[0,1,1]
	v_cmp_eq_u32_e32 vcc, 0, v85
	global_store_dwordx4 v[22:23], v[0:3], off
	s_and_b64 exec, exec, vcc
	s_cbranch_execz .LBB3_39
	s_mov_b32 s0, 0xd000
	v_add_u32_e64 v0, s0, 0
	ds_read2_b64 v[0:3], v0 offset0:100 offset1:108
	v_mov_b32_e32 v9, v5
	v_mov_b32_e32 v5, v11
	v_mov_b32_e32 v8, v10
	v_pk_mov_b32 v[6:7], v[82:83], v[82:83] op_sel:[1,0]
	s_waitcnt lgkmcnt(0)
	v_mov_b32_e32 v15, v1
	v_mov_b32_e32 v1, v3
	v_mov_b32_e32 v14, v2
	v_pk_add_f32 v[0:1], v[4:5], v[0:1]
	v_pk_add_f32 v[8:9], v[8:9], v[14:15]
	v_pk_mul_f32 v[0:1], v[82:83], v[0:1]
	s_nop 0
	v_pk_fma_f32 v[0:1], v[6:7], v[8:9], v[0:1]
	global_store_dwordx2 v[12:13], v[0:1], off offset:32

	.amdhsa_kernel _Z13expert_kernelPKfS0_PKcPf
		.amdhsa_group_segment_fixed_size 78784
		.amdhsa_private_segment_fixed_size 0
		.amdhsa_kernarg_size 32
		.amdhsa_user_sgpr_count 2
		.amdhsa_user_sgpr_dispatch_ptr 0
		.amdhsa_user_sgpr_queue_ptr 0
		.amdhsa_user_sgpr_kernarg_segment_ptr 1
		.amdhsa_user_sgpr_dispatch_id 0
		.amdhsa_user_sgpr_kernarg_preload_length 0
		.amdhsa_user_sgpr_kernarg_preload_offset 0
		.amdhsa_user_sgpr_private_segment_size 0
		.amdhsa_uses_dynamic_stack 0
		.amdhsa_enable_private_segment 0
		.amdhsa_system_sgpr_workgroup_id_x 1
		.amdhsa_system_sgpr_workgroup_id_y 0
		.amdhsa_system_sgpr_workgroup_id_z 0
		.amdhsa_system_sgpr_workgroup_info 0
		.amdhsa_system_vgpr_workitem_id 0
		.amdhsa_next_free_vgpr 256
		.amdhsa_next_free_sgpr 96
		.amdhsa_accum_offset 160
		.amdhsa_reserve_vcc 1
		.amdhsa_float_round_mode_32 0
		.amdhsa_float_round_mode_16_64 0
		.amdhsa_float_denorm_mode_32 3
		.amdhsa_float_denorm_mode_16_64 3
		.amdhsa_dx10_clamp 1
		.amdhsa_ieee_mode 1
		.amdhsa_fp16_overflow 0
		.amdhsa_tg_split 0
		.amdhsa_exception_fp_ieee_invalid_op 0
		.amdhsa_exception_fp_denorm_src 0
		.amdhsa_exception_fp_ieee_div_zero 0
		.amdhsa_exception_fp_ieee_overflow 0
		.amdhsa_exception_fp_ieee_underflow 0
		.amdhsa_exception_fp_ieee_inexact 0
		.amdhsa_exception_int_div_zero 0
	.end_amdhsa_kernel

amdhsa.kernels:
  - .agpr_count:     0
    .args:
      - .actual_access:  read_only
        .address_space:  global
        .offset:         0
        .size:           8
        .value_kind:     global_buffer
      - .actual_access:  read_only
        .address_space:  global
        .offset:         8
        .size:           8
        .value_kind:     global_buffer
      - .actual_access:  read_only
        .address_space:  global
        .offset:         16
        .size:           8
        .value_kind:     global_buffer
      - .actual_access:  read_only
        .address_space:  global
        .offset:         24
        .size:           8
        .value_kind:     global_buffer
      - .actual_access:  write_only
        .address_space:  global
        .offset:         32
        .size:           8
        .value_kind:     global_buffer
    .group_segment_fixed_size: 0
    .kernarg_segment_align: 8
    .kernarg_segment_size: 40
    .language:       OpenCL C
    .language_version:
      - 2
      - 0
    .max_flat_workgroup_size: 256
    .name:           _Z11prep_kernelPKfS0_S0_S0_Pc
    .private_segment_fixed_size: 0
    .sgpr_count:     30
    .sgpr_spill_count: 0
    .symbol:         _Z11prep_kernelPKfS0_S0_S0_Pc.kd
    .uniform_work_group_size: 1
    .uses_dynamic_stack: false
    .vgpr_count:     20
    .vgpr_spill_count: 0
    .wavefront_size: 64
  - .agpr_count:     0
    .args:
      - .address_space:  global
        .offset:         0
        .size:           8
        .value_kind:     global_buffer
      - .actual_access:  read_only
        .address_space:  global
        .offset:         8
        .size:           8
        .value_kind:     global_buffer
      - .actual_access:  read_only
        .address_space:  global
        .offset:         16
        .size:           8
        .value_kind:     global_buffer
      - .address_space:  global
        .offset:         24
        .size:           8
        .value_kind:     global_buffer
      - .actual_access:  write_only
        .address_space:  global
        .offset:         32
        .size:           8
        .value_kind:     global_buffer
      - .address_space:  global
        .offset:         40
        .size:           8
        .value_kind:     global_buffer
    .group_segment_fixed_size: 133120
    .kernarg_segment_align: 8
    .kernarg_segment_size: 48
    .language:       OpenCL C
    .language_version:
      - 2
      - 0
    .max_flat_workgroup_size: 512
    .name:           _Z13router_kernelPKfS0_S0_PcPfS1_
    .private_segment_fixed_size: 0
    .sgpr_count:     106
    .sgpr_spill_count: 7
    .symbol:         _Z13router_kernelPKfS0_S0_PcPfS1_.kd
    .uniform_work_group_size: 1
    .uses_dynamic_stack: false
    .vgpr_count:     239
    .vgpr_spill_count: 0
    .wavefront_size: 64
  - .agpr_count:     0
    .args:
      - .address_space:  global
        .offset:         0
        .size:           8
        .value_kind:     global_buffer
    .group_segment_fixed_size: 20
    .kernarg_segment_align: 8
    .kernarg_segment_size: 8
    .language:       OpenCL C
    .language_version:
      - 2
      - 0
    .max_flat_workgroup_size: 320
    .name:           _Z11plan_kernelPc
    .private_segment_fixed_size: 0
    .sgpr_count:     16
    .sgpr_spill_count: 0
    .symbol:         _Z11plan_kernelPc.kd
    .uniform_work_group_size: 1
    .uses_dynamic_stack: false
    .vgpr_count:     20
    .vgpr_spill_count: 0
    .wavefront_size: 64
  - .agpr_count:     96
    .args:
      - .actual_access:  read_only
        .address_space:  global
        .offset:         0
        .size:           8
        .value_kind:     global_buffer
      - .actual_access:  read_only
        .address_space:  global
        .offset:         8
        .size:           8
        .value_kind:     global_buffer
      - .address_space:  global
        .offset:         16
        .size:           8
        .value_kind:     global_buffer
      - .actual_access:  write_only
        .address_space:  global
        .offset:         24
        .size:           8
        .value_kind:     global_buffer
    .group_segment_fixed_size: 78784
    .kernarg_segment_align: 8
    .kernarg_segment_size: 32
    .language:       OpenCL C
    .language_version:
      - 2
      - 0
    .max_flat_workgroup_size: 256
    .name:           _Z13expert_kernelPKfS0_PKcPf
    .private_segment_fixed_size: 0
    .sgpr_count:     36
    .sgpr_spill_count: 0
    .symbol:         _Z13expert_kernelPKfS0_PKcPf.kd
    .uniform_work_group_size: 1
    .uses_dynamic_stack: false
    .vgpr_count:     256
    .vgpr_spill_count: 0
    .wavefront_size: 64
